# dma1: sa1 + attention K/V tiles staged global->LDS directly (global_load_lds_dwordx4 with swizzle carried by the per-lane source offsets) instead of via VGPRs + ds_write
# speedup vs baseline: 1.0097x; 1.0093x over previous
; __device__ __forceinline__ int v_st(int k, int c) { const int kk = (k & ~0xC) | ((k & 4) << 1) | ((k & 8) >> 1); return ((kk >> 3) * 4 + (c >> 5)) * 512 + ((kk & 7) * 32 + (c & 31)) * 2; }
; __device__ __forceinline__ int v_rd_base(int lane) { return ((lane & 3) << 3) | (((lane >> 2) & 3) << 6) | (((lane >> 4) & 1) << 5) | (((lane >> 5) & 1) << 8); }
; #define SLOAD(k0) do { vs0 = *reinterpret_cast<const bf16x8*>(&Vh[(size_t)((k0) + sr) * DM + sc]); vs1 = *reinterpret_cast<const bf16x8*>(&Vh[(size_t)((k0) + 32 + sr) * DM + sc]); \
;     ks = *reinterpret_cast<const bf16x8*>(&Kh[(size_t)((k0) + kr) * DM + kc]); } while (0)
; #define SWRITE(s) do { *(bf16x8*)(V_lds + (s) * SHM_V + vst0) = vs0; *(bf16x8*)(V_lds + (s) * SHM_V + vst1) = vs1; *(bf16x8*)(K_lds + (s) * SHM_K64 + kst) = ks; } while (0)
; __device__ __forceinline__ void diff_pass(const bf16_t* __restrict__ Qb, const bf16_t* __restrict__ Kh, const bf16_t* __restrict__ Vh, int seq, char* lds, f32x16 (&o)[4], const int wave_) {
;     ...
;     const bf16_t* Qw = Qb + (size_t)(wid * 32 + r32) * DM + hi * 8;
; #pragma unroll
;     for (int d0 = 0; d0 < 4; ++d0) qr[d0] = *reinterpret_cast<const bf16x8*>(Qw + d0 * 16);
;     const int sr = tid >> 4, sc = (tid & 15) * 8, vst0 = v_st(sr, sc), vst1 = v_st(32 + sr, sc);
;     const int kr = tid >> 3, kc = (tid & 7) * 8, kst = kswz<64>(kr, kc * 2);
;     const int vb0 = (int)(uintptr_t)V_lds + v_rd_base(lane);
;     bf16x8 vs0, vs1, ks;
;     ...
;     __syncthreads();
;     SLOAD(0); SWRITE(0); SLOAD(64); __syncthreads();
.LBB0_822:
	s_lshl_b32 s0, s36, 1
	s_mov_b32 s1, -1
	s_and_b32 s64, s0, 0x700
	s_ashr_i32 s0, s37, 6
	s_lshl_b32 s2, s37, 8
	v_mbcnt_lo_u32_b32 v0, s1, 0
	v_mbcnt_hi_u32_b32 v0, s1, v0
	s_ashr_i32 s1, s0, 31
	s_lshl_b64 s[6:7], s[0:1], 11
	s_and_b32 s2, s2, 0x700
	s_or_b32 s6, s6, s2
	s_lshl_b64 s[2:3], s[6:7], 11
	v_readlane_b32 s8, v252, 16
	v_readlane_b32 s9, v252, 17
	s_add_u32 s2, s8, s2
	s_addc_u32 s3, s9, s3
	s_lshl_b32 s8, s37, 4
	s_and_b32 s38, s8, 0x380
	s_lshl_b32 s8, s38, 1
	s_add_u32 s34, s2, s8
	s_addc_u32 s35, s3, 0
	s_lshl_b64 s[10:11], s[0:1], 22
	v_readlane_b32 s0, v251, 42
	s_add_u32 s0, s0, s10
	v_readlane_b32 s1, v251, 43
	s_addc_u32 s1, s1, s11
	s_add_u32 s28, s0, s8
	s_addc_u32 s29, s1, 0
	v_readlane_b32 s0, v251, 44
	s_add_u32 s0, s0, s10
	v_readlane_b32 s1, v251, 45
	s_addc_u32 s1, s1, s11
	v_or_b32_e32 v207, s55, v0
	s_add_u32 s30, s0, s8
	s_mov_b32 s0, -1
	s_addc_u32 s31, s1, 0
	v_mbcnt_lo_u32_b32 v0, s0, 0
	v_mbcnt_hi_u32_b32 v0, s0, v0
	v_or_b32_e32 v68, s55, v0
	s_movk_i32 s0, 0xffe0
	v_ashrrev_i32_e32 v0, 1, v68
	v_bfi_b32 v0, s0, v0, v68
	v_ashrrev_i32_e32 v1, 31, v0
	v_lshlrev_b64 v[0:1], 11, v[0:1]
	v_lshrrev_b32_e32 v2, 1, v68
	v_ashrrev_i32_e32 v12, 4, v68
	v_lshl_add_u64 v[0:1], s[34:35], 0, v[0:1]
	v_and_b32_e32 v160, 16, v2
	v_lshlrev_b32_e32 v24, 3, v68
	v_ashrrev_i32_e32 v13, 31, v12
	v_lshl_add_u64 v[0:1], v[0:1], 0, v[160:161]
	v_and_b32_e32 v2, 0x78, v24
	v_lshlrev_b64 v[48:49], 11, v[12:13]
	global_load_dwordx4 v[162:165], v[0:1], off
	global_load_dwordx4 v[166:169], v[0:1], off offset:32
	global_load_dwordx4 v[170:173], v[0:1], off offset:64
	global_load_dwordx4 v[174:177], v[0:1], off offset:96
	v_lshl_add_u64 v[0:1], s[30:31], 0, v[48:49]
	v_lshlrev_b32_e32 v4, 1, v2
	v_mov_b32_e32 v5, v161
	v_add_u32_e32 v14, 32, v12
	v_ashrrev_i32_e32 v16, 3, v68
	v_lshl_add_u64 v[18:19], v[0:1], 0, v[4:5]
	s_barrier
	global_load_dwordx4 v[0:3], v[18:19], off
	v_ashrrev_i32_e32 v15, 31, v14
	v_ashrrev_i32_e32 v17, 31, v16
	v_lshlrev_b32_e32 v64, 4, v68
	v_lshlrev_b64 v[6:7], 11, v[14:15]
	v_lshlrev_b64 v[50:51], 11, v[16:17]
	v_lshl_add_u64 v[6:7], s[30:31], 0, v[6:7]
	v_and_b32_e32 v20, 0x70, v64
	v_lshl_add_u64 v[8:9], s[28:29], 0, v[50:51]
	v_mov_b32_e32 v21, v161
	v_lshl_add_u64 v[4:5], v[6:7], 0, v[4:5]
	v_lshl_add_u64 v[22:23], v[8:9], 0, v[20:21]
	global_load_dwordx4 v[4:7], v[4:5], off
	v_and_b32_e32 v13, 0xfffff0, v12
	global_load_dwordx4 v[8:11], v[22:23], off
	v_add_co_u32_e32 v194, vcc, 0x20000, v18
	s_nop 1
	v_addc_co_u32_e32 v195, vcc, 0, v19, vcc
	global_load_dwordx4 v[52:55], v[194:195], off
	v_add_co_u32_e32 v194, vcc, 0x30000, v18
	s_nop 1
	v_addc_co_u32_e32 v195, vcc, 0, v19, vcc
	global_load_dwordx4 v[56:59], v[194:195], off
	v_add_co_u32_e32 v194, vcc, 0x20000, v22
	s_nop 1
	v_addc_co_u32_e32 v195, vcc, 0, v23, vcc
	global_load_dwordx4 v[60:63], v[194:195], off
	v_lshlrev_b32_e32 v15, 1, v12
	v_and_or_b32 v13, v15, 8, v13
	v_lshrrev_b32_e32 v15, 1, v12
	v_lshrrev_b32_e32 v13, 1, v13
	v_bfe_u32 v17, v24, 5, 2
	v_and_b32_e32 v12, 3, v12
	v_or_b32_e32 v13, v13, v17
	v_and_or_b32 v12, v15, 4, v12
	v_lshlrev_b32_e32 v13, 9, v13
	v_lshlrev_b32_e32 v12, 6, v12
	v_and_b32_e32 v15, 48, v64
	v_or3_b32 v218, v13, v12, v15
	v_and_b32_e32 v13, 0xfffff0, v14
	v_lshlrev_b32_e32 v14, 1, v14
	v_and_or_b32 v13, v14, 8, v13
	v_lshrrev_b32_e32 v13, 1, v13
	v_or_b32_e32 v13, v13, v17
	v_add_u32_e32 v70, 0, v218
	s_mov_b32 s0, 0x20000
	v_lshlrev_b32_e32 v13, 9, v13
	v_or3_b32 v219, v13, v12, v15
	v_lshlrev_b32_e32 v12, 7, v16
	v_and_b32_e32 v13, 0x70, v68
	s_mov_b32 s1, 0x30000
	v_bitop3_b32 v220, v20, v12, v13 bitop3:0xde
	v_add_u32_e32 v71, 0, v219
	v_add_u32_e32 v221, 0, v220
	v_and_b32_e32 v69, 31, v68
	v_lshlrev_b32_e32 v12, 7, v69
	v_and_b32_e32 v13, 0x70, v24
	v_bitop3_b32 v223, v160, v12, v13 bitop3:0xde
	v_add_u32_e32 v222, 0, v223
	s_add_i32 s39, 0, 0x12000
	v_and_b32_e32 v72, 63, v68
	s_mov_b32 s12, 0
	s_mov_b32 s13, s12
	s_mov_b32 s14, s12
	s_mov_b32 s15, s12
	s_mov_b32 s16, s12
	s_mov_b32 s17, s12
	s_mov_b32 s18, s12
	s_mov_b32 s19, s12
	s_mov_b32 s20, s12
	s_mov_b32 s21, s12
	s_mov_b32 s22, s12
	s_mov_b32 s23, s12
	s_mov_b32 s24, s12
	s_mov_b32 s25, s12
	s_mov_b32 s26, s12
	s_mov_b32 s27, s12
	s_cmp_lg_u32 0, -1
	s_mov_b32 s42, 1
	s_mov_b32 s40, -1
	s_mov_b32 s41, 2
	v_mov_b32_e32 v230, 1.0
	v_mov_b32_e32 v215, 0
	s_waitcnt vmcnt(5)
	ds_write_b128 v70, v[0:3]
	s_waitcnt vmcnt(4)
	ds_write_b128 v71, v[4:7]
	s_waitcnt vmcnt(3)
	ds_write_b128 v221, v[8:11] offset:49152
	v_and_b32_e32 v8, 0x3fffffc0, v68
	s_waitcnt lgkmcnt(0)
	s_barrier
	ds_read_b128 v[0:3], v222 offset:49152
	ds_read_b128 v[4:7], v222 offset:53248
	s_waitcnt lgkmcnt(1)
	v_mfma_f32_32x32x16_bf16 v[16:31], v[0:3], v[162:165], 0
	v_or_b32_e32 v0, 32, v160
	v_bitop3_b32 v226, v0, v12, v13 bitop3:0xde
	v_add_u32_e32 v224, 0, v226
	ds_read_b128 v[0:3], v224 offset:49152
	v_lshl_add_u32 v213, v8, 2, s39
	s_cselect_b32 s0, 0, 0
	v_lshl_add_u32 v214, v69, 2, v213
	s_waitcnt lgkmcnt(1)
	v_mfma_f32_32x32x16_bf16 v[32:47], v[4:7], v[162:165], 0
	ds_read_b128 v[4:7], v224 offset:53248
	s_waitcnt lgkmcnt(1)
	v_mfma_f32_32x32x16_bf16 v[16:31], v[0:3], v[166:169], v[16:31]
	v_or_b32_e32 v0, 64, v160
	v_bitop3_b32 v228, v0, v12, v13 bitop3:0xde
	v_add_u32_e32 v225, 0, v228
	ds_read_b128 v[0:3], v225 offset:53248
	ds_read_b128 v[8:11], v225 offset:49152
	s_waitcnt lgkmcnt(2)
	v_mfma_f32_32x32x16_bf16 v[32:47], v[4:7], v[166:169], v[32:47]
	v_lshlrev_b32_e32 v4, 3, v72
	v_and_b32_e32 v5, 0xc0, v64
	v_lshlrev_b32_e32 v6, 1, v68
	v_and_or_b32 v5, v4, 24, v5
	v_and_b32_e32 v6, 32, v6
	v_and_b32_e32 v4, 0x100, v4
	v_or3_b32 v216, v5, v6, v4
	s_waitcnt lgkmcnt(0)
	v_mfma_f32_32x32x16_bf16 v[16:31], v[8:11], v[170:173], v[16:31]
	v_or_b32_e32 v4, 0x60, v160
	v_bitop3_b32 v229, v4, v12, v13 bitop3:0xde
	v_add_u32_e32 v227, 0, v229
	ds_read_b128 v[64:67], v227 offset:53248
	ds_read_b128 v[4:7], v227 offset:49152
	s_waitcnt vmcnt(2)
	ds_write_b128 v70, v[52:55] offset:16384
	s_waitcnt vmcnt(1)
	ds_write_b128 v71, v[56:59] offset:16384
	s_waitcnt vmcnt(0)
	ds_write_b128 v221, v[60:63] offset:57344
	v_mfma_f32_32x32x16_bf16 v[32:47], v[0:3], v[170:173], v[32:47]
	v_add_u32_e32 v217, s0, v216
	v_cmp_gt_u32_e64 s[0:1], 32, v72
	s_waitcnt lgkmcnt(0)
	s_barrier
; #define SWRITE(s) do { *(bf16x8*)(V_lds + (s) * SHM_V + vst0) = vs0; *(bf16x8*)(V_lds + (s) * SHM_V + vst1) = vs1; *(bf16x8*)(K_lds + (s) * SHM_K64 + kst) = ks; } while (0)
; #define ROT() do { s_prev = s_cur; s_cur = s_next; s_next = (s_next == DA_NBUF - 1) ? 0 : s_next + 1; } while (0)
; #define EX2(x) x = __builtin_amdgcn_exp2f(x)
; __device__ __forceinline__ void diff_pass(const bf16_t* __restrict__ Qb, const bf16_t* __restrict__ Kh, const bf16_t* __restrict__ Vh, int seq, char* lds, f32x16 (&o)[4], const int wave_) {
;     ...
;     negm = f32x16{};
;     qkt64c(pA0, pA1, K_lds, qr, negm, r32, hi);
;     { const float pm = rowmax32(pA0, pA1); m_reg = pm; alA = 1.f;
; #pragma unroll
;       for (int r = 0; r < 16; ++r) { pA0[r] -= pm; pA1[r] -= pm; negm[r] = -pm; }
; #pragma unroll
;       for (int r = 0; r < 16; ++r) EX2(pA0[r]);
; #pragma unroll
;       for (int r = 0; r < 8; ++r) EX2(pA1[r]); }
;     SWRITE(1); __syncthreads();
;     ROT();
	v_mfma_f32_32x32x16_bf16 v[16:31], v[4:7], v[174:177], v[16:31]
	v_mov_b64_e32 v[0:1], s[12:13]
	v_mov_b64_e32 v[14:15], s[26:27]
	v_mov_b64_e32 v[2:3], s[14:15]
	v_mov_b64_e32 v[4:5], s[16:17]
	v_mov_b64_e32 v[6:7], s[18:19]
	v_mov_b64_e32 v[8:9], s[20:21]
	v_mov_b64_e32 v[10:11], s[22:23]
	v_mfma_f32_32x32x16_bf16 v[32:47], v[64:67], v[174:177], v[32:47]
	s_nop 3
	v_max_f32_e32 v64, v17, v17
	v_max_f32_e32 v65, v16, v16
	v_max_f32_e32 v64, v65, v64
	v_mov_b64_e32 v[12:13], s[24:25]
	s_nop 3
	v_max3_f32 v65, v18, v19, v33
	v_max3_f32 v64, v64, v32, v34
	v_max3_f32 v64, v64, v35, v20
	v_max3_f32 v65, v65, v22, v23
	v_max3_f32 v64, v64, v21, v36
	v_max3_f32 v65, v65, v38, v39
	v_max3_f32 v64, v64, v37, v24
	v_max3_f32 v65, v65, v26, v27
	v_max3_f32 v64, v64, v25, v40
	v_max3_f32 v65, v65, v42, v43
	v_max3_f32 v64, v64, v41, v28
	v_max3_f32 v65, v65, v30, v31
	v_max3_f32 v64, v64, v29, v44
	v_max3_f32 v65, v65, v46, v47
	v_max3_f32 v64, v64, v45, v65
	v_mov_b32_e32 v65, v64
	s_nop 1
	v_permlane32_swap_b32_e32 v64, v65
	v_max_f32_e32 v65, v65, v65
	v_max_f32_e32 v64, v64, v64
	v_max_f32_e32 v196, v64, v65
	v_sub_f32_e32 v16, v16, v196
	v_sub_f32_e32 v17, v17, v196
	v_sub_f32_e32 v18, v18, v196
	v_exp_f32_e32 v96, v16
	v_exp_f32_e32 v97, v17
	v_exp_f32_e32 v98, v18
	v_lshl_add_u64 v[16:17], s[10:11], 0, v[50:51]
	v_and_b32_e32 v18, 7, v68
	v_sub_f32_e32 v32, v32, v196
	v_sub_f32_e32 v33, v33, v196
	v_sub_f32_e32 v34, v34, v196
	v_sub_f32_e32 v19, v19, v196
	v_sub_f32_e32 v35, v35, v196
	v_sub_f32_e32 v20, v20, v196
	v_sub_f32_e32 v36, v36, v196
	v_sub_f32_e32 v21, v21, v196
	v_sub_f32_e32 v37, v37, v196
	v_sub_f32_e32 v22, v22, v196
	v_sub_f32_e32 v38, v38, v196
	v_sub_f32_e32 v23, v23, v196
	v_sub_f32_e32 v39, v39, v196
	v_sub_f32_e32 v24, v24, v196
	v_sub_f32_e32 v25, v25, v196
	v_sub_f32_e32 v26, v26, v196
	v_sub_f32_e32 v27, v27, v196
	v_sub_f32_e32 v28, v28, v196
	v_sub_f32_e32 v29, v29, v196
	v_sub_f32_e32 v30, v30, v196
	v_sub_f32_e32 v31, v31, v196
	v_lshl_or_b32 v16, v18, 4, v16
	v_exp_f32_e32 v99, v19
	v_exp_f32_e32 v100, v20
	v_exp_f32_e32 v101, v21
	v_exp_f32_e32 v102, v22
	v_exp_f32_e32 v103, v23
	v_exp_f32_e32 v104, v24
	v_exp_f32_e32 v105, v25
	v_exp_f32_e32 v106, v26
	v_exp_f32_e32 v107, v27
	v_exp_f32_e32 v108, v28
	v_exp_f32_e32 v109, v29
	v_exp_f32_e32 v110, v30
	v_exp_f32_e32 v111, v31
	v_exp_f32_e32 v112, v32
	v_exp_f32_e32 v113, v33
	v_exp_f32_e32 v114, v34
	v_exp_f32_e32 v115, v35
	v_exp_f32_e32 v116, v36
	v_exp_f32_e32 v117, v37
	v_exp_f32_e32 v118, v38
	v_exp_f32_e32 v119, v39
	v_lshl_add_u64 v[198:199], s[52:53], 0, v[16:17]
	v_lshl_add_u64 v[16:17], s[10:11], 0, v[48:49]
	v_and_b32_e32 v18, 15, v68
	v_lshl_or_b32 v16, v18, 4, v16
	v_xor_b32_e32 v80, 0x80000000, v196
	v_pk_add_f32 v[120:121], v[40:41], v[196:197] op_sel_hi:[1,0] neg_lo:[0,1] neg_hi:[0,1]
	v_pk_add_f32 v[122:123], v[42:43], v[196:197] op_sel_hi:[1,0] neg_lo:[0,1] neg_hi:[0,1]
	v_pk_add_f32 v[124:125], v[44:45], v[196:197] op_sel_hi:[1,0] neg_lo:[0,1] neg_hi:[0,1]
	v_pk_add_f32 v[126:127], v[46:47], v[196:197] op_sel_hi:[1,0] neg_lo:[0,1] neg_hi:[0,1]
	v_lshl_add_u64 v[200:201], s[52:53], 0, v[16:17]
	s_add_u32 s14, s52, s10
	s_addc_u32 s15, s53, s11
	s_add_u32 s14, s14, s64
	s_addc_u32 s15, s15, s65
	s_add_u32 s16, s14, 0x8a40000
	s_addc_u32 s17, s15, 0
	s_add_u32 s14, s14, 0x6a40000
	s_addc_u32 s15, s15, 0
	s_lshl_b32 s18, s55, 4
	v_lshrrev_b32_e32 v194, 4, v207
	v_xor_b32_e32 v194, v194, v207
	v_and_b32_e32 v194, 7, v194
	v_lshrrev_b32_e32 v195, 3, v207
	v_lshlrev_b32_e32 v195, 11, v195
	v_lshl_or_b32 v194, v194, 4, v195
	v_lshrrev_b32_e32 v195, 2, v207
	v_and_b32_e32 v195, 7, v195
	v_and_b32_e32 v255, 3, v195
	v_lshrrev_b32_e32 v195, 2, v195
	v_lshl_or_b32 v255, v195, 3, v255
	v_lshrrev_b32_e32 v195, 7, v207
	v_and_b32_e32 v195, 1, v195
	v_lshl_or_b32 v255, v195, 2, v255
	v_lshrrev_b32_e32 v195, 8, v207
	v_lshl_or_b32 v255, v195, 4, v255
	v_lshlrev_b32_e32 v255, 11, v255
	v_lshrrev_b32_e32 v195, 5, v207
	v_and_b32_e32 v195, 3, v195
	v_lshl_or_b32 v255, v195, 6, v255
	v_and_b32_e32 v195, 3, v207
	v_lshl_or_b32 v195, v195, 4, v255
	v_add_u32_e32 v255, 0x10000, v195
	v_mov_b64_e32 v[62:63], v[14:15]
	v_mov_b64_e32 v[46:47], v[14:15]
	v_mov_b64_e32 v[30:31], v[14:15]
	v_mov_b64_e32 v[60:61], v[12:13]
	v_mov_b64_e32 v[58:59], v[10:11]
	v_mov_b64_e32 v[56:57], v[8:9]
	v_mov_b64_e32 v[54:55], v[6:7]
	v_mov_b64_e32 v[52:53], v[4:5]
	v_mov_b64_e32 v[50:51], v[2:3]
	v_mov_b64_e32 v[48:49], v[0:1]
	v_mov_b64_e32 v[44:45], v[12:13]
	v_mov_b64_e32 v[42:43], v[10:11]
	v_mov_b64_e32 v[40:41], v[8:9]
	v_mov_b64_e32 v[38:39], v[6:7]
	v_mov_b64_e32 v[36:37], v[4:5]
	v_mov_b64_e32 v[34:35], v[2:3]
	v_mov_b64_e32 v[32:33], v[0:1]
	v_mov_b64_e32 v[28:29], v[12:13]
	v_mov_b64_e32 v[26:27], v[10:11]
	v_mov_b64_e32 v[24:25], v[8:9]
	v_mov_b64_e32 v[22:23], v[6:7]
	v_mov_b64_e32 v[20:21], v[4:5]
	v_mov_b64_e32 v[18:19], v[2:3]
	v_mov_b64_e32 v[16:17], v[0:1]
	v_mov_b32_e32 v81, v80
	v_mov_b32_e32 v82, v80
	v_mov_b32_e32 v83, v80
	v_mov_b32_e32 v84, v80
	v_mov_b32_e32 v85, v80
	v_mov_b32_e32 v86, v80
	v_mov_b32_e32 v87, v80
	v_mov_b32_e32 v88, v80
	v_mov_b32_e32 v89, v80
	v_mov_b32_e32 v90, v80
	v_mov_b32_e32 v91, v80
	v_mov_b32_e32 v92, v80
	v_mov_b32_e32 v93, v80
	v_mov_b32_e32 v94, v80
	v_mov_b32_e32 v95, v80

; #define SBAR() __builtin_amdgcn_sched_barrier(0)
; #define SLOAD(k0) do { vs0 = *reinterpret_cast<const bf16x8*>(&Vh[(size_t)((k0) + sr) * DM + sc]); vs1 = *reinterpret_cast<const bf16x8*>(&Vh[(size_t)((k0) + 32 + sr) * DM + sc]); \
;     ks = *reinterpret_cast<const bf16x8*>(&Kh[(size_t)((k0) + kr) * DM + kc]); } while (0)
; __device__ __forceinline__ void diff_pass(const bf16_t* __restrict__ Qb, const bf16_t* __restrict__ Kh, const bf16_t* __restrict__ Vh, int seq, char* lds, f32x16 (&o)[4], const int wave_) {
;     ...
;     for (int j = 1; j + 1 < NT; j += 2) {
;         SLOAD((j + 1) * 64);
;         SBAR(); qkt64c(pB0, pB1, K_lds + s_cur * SHM_K64, qr, negm, r32, hi); FIN(pA0, pA1, alA); SBAR();
;         YSEG(pB0, pB1, alB, s_prev);
.Latt9_p1_top:
	ds_read_b128 v[144:147], v128 offset:49152
	ds_read_b128 v[148:151], v129 offset:49152
	ds_read_b128 v[152:155], v130 offset:49152
	ds_read_b128 v[156:159], v131 offset:49152
	ds_read_b128 v[232:235], v128 offset:53248
	ds_read_b128 v[236:239], v129 offset:53248
	ds_read_b128 v[240:243], v130 offset:53248
	ds_read_b128 v[244:247], v131 offset:53248
	s_lshl_b32 s19, s41, 14
	s_add_i32 s19, s19, s18
	s_mov_b32 m0, s19
	s_lshl_b32 s20, s41, 13
	global_load_lds_dwordx4 v195, s[16:17]
	s_add_i32 m0, s19, 0x2000
	s_add_i32 s20, s20, s18
	global_load_lds_dwordx4 v255, s[16:17]
	s_add_i32 m0, s20, 0xc000
	s_add_u32 s16, s16, 0x20000
	global_load_lds_dwordx4 v194, s[14:15]
	s_addc_u32 s17, s17, 0
	s_add_u32 s14, s14, 0x20000
	s_addc_u32 s15, s15, 0
	v_exp_f32_e32 v190, v120
	v_exp_f32_e32 v191, v121
	v_add_f32_e32 v120, v96, v97
	v_add_f32_e32 v121, v98, v99
	s_waitcnt lgkmcnt(7)
	v_mfma_f32_32x32x16_bf16 v[128:143], v[144:147], v[162:165], v[80:95]
	v_exp_f32_e32 v192, v122
	v_add_f32_e32 v120, v120, v121
	v_add_f32_e32 v121, v100, v101
	v_add_f32_e32 v122, v102, v103
	v_exp_f32_e32 v193, v123
	s_waitcnt lgkmcnt(6)
	v_mfma_f32_32x32x16_bf16 v[128:143], v[148:151], v[166:169], v[128:143]
	v_add_f32_e32 v121, v121, v122
	v_add_f32_e32 v122, v104, v105
	v_add_f32_e32 v123, v106, v107
	v_add_f32_e32 v122, v122, v123
	v_add_f32_e32 v123, v108, v109
	s_waitcnt lgkmcnt(5)
	v_mfma_f32_32x32x16_bf16 v[128:143], v[152:155], v[170:173], v[128:143]
	v_add_f32_e32 v208, v110, v111
	v_add_f32_e32 v123, v123, v208
	v_add_f32_e32 v208, v112, v113
	v_add_f32_e32 v209, v114, v115
	v_add_f32_e32 v208, v208, v209
	s_waitcnt lgkmcnt(4)
	v_mfma_f32_32x32x16_bf16 v[128:143], v[156:159], v[174:177], v[128:143]
	v_exp_f32_e32 v124, v124
	v_exp_f32_e32 v125, v125
	s_waitcnt lgkmcnt(3)
	v_mfma_f32_32x32x16_bf16 v[144:159], v[232:235], v[162:165], v[80:95]
	v_lshl_add_u32 v234, s12, 14, v217
	ds_read_b64_tr_b16 v[64:65], v234 offset:0
	ds_read_b64_tr_b16 v[66:67], v234 offset:0x800
	ds_read_b64_tr_b16 v[68:69], v234 offset:0x1000
	ds_read_b64_tr_b16 v[70:71], v234 offset:0x1800
	ds_read_b64_tr_b16 v[72:73], v234 offset:0x2000
	ds_read_b64_tr_b16 v[74:75], v234 offset:0x2800
	ds_read_b64_tr_b16 v[76:77], v234 offset:0x3000
	ds_read_b64_tr_b16 v[78:79], v234 offset:0x3800
	v_exp_f32_e32 v126, v126
	v_exp_f32_e32 v127, v127
	v_add_f32_e32 v120, v208, v120
	v_add_f32_e32 v208, v116, v117
	v_add_f32_e32 v209, v118, v119
	v_add_f32_e32 v208, v208, v209
	v_add_f32_e32 v121, v208, v121
	s_waitcnt lgkmcnt(10)
	v_mfma_f32_32x32x16_bf16 v[144:159], v[236:239], v[166:169], v[144:159]
	v_add_f32_e32 v208, v190, v191
	v_add_f32_e32 v209, v192, v193
	v_add_f32_e32 v208, v208, v209
	v_add_f32_e32 v122, v122, v208
	v_add_f32_e32 v208, v124, v125
	v_add_f32_e32 v209, v126, v127
	v_add_f32_e32 v208, v208, v209
	s_waitcnt lgkmcnt(9)
	v_mfma_f32_32x32x16_bf16 v[144:159], v[240:243], v[170:173], v[144:159]
	v_add_f32_e32 v123, v123, v208
	v_add_f32_e32 v120, v120, v121
	v_add_f32_e32 v121, v122, v123
	v_add_f32_e32 v231, v120, v121
	v_mov_b32_e32 v232, v231
	v_cvt_pk_bf16_f32 v96, v96, v97
	v_cvt_pk_bf16_f32 v97, v98, v99
	s_waitcnt lgkmcnt(8)
	v_mfma_f32_32x32x16_bf16 v[144:159], v[244:247], v[174:177], v[144:159]
	v_cvt_pk_bf16_f32 v98, v100, v101
	v_cvt_pk_bf16_f32 v99, v102, v103
	v_cvt_pk_bf16_f32 v120, v104, v105
	v_cvt_pk_bf16_f32 v121, v106, v107
	v_cvt_pk_bf16_f32 v122, v108, v109
	v_cvt_pk_bf16_f32 v123, v110, v111
	v_permlane32_swap_b32_e32 v96, v98
	v_permlane32_swap_b32_e32 v97, v99
	v_cvt_pk_bf16_f32 v104, v112, v113
	v_cvt_pk_bf16_f32 v105, v114, v115
	v_cvt_pk_bf16_f32 v106, v116, v117
	v_cvt_pk_bf16_f32 v107, v118, v119
	s_waitcnt lgkmcnt(0)
	v_mfma_f32_32x32x16_bf16 v[0:15], v[96:99], v[64:67], v[0:15]
	v_permlane32_swap_b32_e32 v120, v122
	v_permlane32_swap_b32_e32 v121, v123
	v_cvt_pk_bf16_f32 v100, v190, v191
	v_cvt_pk_bf16_f32 v101, v192, v193
	v_cvt_pk_bf16_f32 v102, v124, v125
	v_cvt_pk_bf16_f32 v103, v126, v127
	v_mfma_f32_32x32x16_bf16 v[0:15], v[120:123], v[68:71], v[0:15]
	v_permlane32_swap_b32_e32 v104, v106
	v_permlane32_swap_b32_e32 v105, v107
	ds_read_b64_tr_b16 v[236:237], v234 offset:0x200
	ds_read_b64_tr_b16 v[238:239], v234 offset:0xa00
	ds_read_b64_tr_b16 v[240:241], v234 offset:0x1200
	ds_read_b64_tr_b16 v[242:243], v234 offset:0x1a00
	ds_read_b64_tr_b16 v[244:245], v234 offset:0x2200
	ds_read_b64_tr_b16 v[246:247], v234 offset:0x2a00
	ds_read_b64_tr_b16 v[190:191], v234 offset:0x3200
	ds_read_b64_tr_b16 v[192:193], v234 offset:0x3a00
	v_mfma_f32_32x32x16_bf16 v[0:15], v[104:107], v[72:75], v[0:15]
	v_permlane32_swap_b32_e32 v100, v102
	v_permlane32_swap_b32_e32 v101, v103
	v_permlane32_swap_b32_e32 v231, v232
	v_max_f32_e32 v108, v128, v129
	v_max3_f32 v109, v130, v131, v145
	v_max3_f32 v108, v108, v144, v146
	v_max3_f32 v108, v108, v147, v132
	v_max3_f32 v109, v109, v134, v135
	v_mfma_f32_32x32x16_bf16 v[0:15], v[100:103], v[76:79], v[0:15]
	v_max3_f32 v208, v108, v133, v148
	v_max3_f32 v209, v109, v150, v151
	ds_read_b64_tr_b16 v[124:125], v234 offset:0x400
	ds_read_b64_tr_b16 v[126:127], v234 offset:0xc00
	ds_read_b64_tr_b16 v[116:117], v234 offset:0x1400
	ds_read_b64_tr_b16 v[118:119], v234 offset:0x1c00
	ds_read_b64_tr_b16 v[112:113], v234 offset:0x2400
	ds_read_b64_tr_b16 v[114:115], v234 offset:0x2c00
	ds_read_b64_tr_b16 v[108:109], v234 offset:0x3400
	ds_read_b64_tr_b16 v[110:111], v234 offset:0x3c00
	s_waitcnt lgkmcnt(8)
	v_mfma_f32_32x32x16_bf16 v[48:63], v[96:99], v[236:239], v[48:63]
	v_max3_f32 v208, v208, v149, v136
	v_max3_f32 v209, v209, v138, v139
	v_max3_f32 v208, v208, v137, v152
	v_max3_f32 v209, v209, v154, v155
	v_max3_f32 v208, v208, v153, v140
	v_max3_f32 v209, v209, v142, v143
	v_max3_f32 v208, v208, v141, v156
	v_mfma_f32_32x32x16_bf16 v[48:63], v[120:123], v[240:243], v[48:63]
	v_max3_f32 v209, v209, v158, v159
	v_max3_f32 v208, v208, v157, v209
	v_mov_b32_e32 v209, v208
	s_nop 1
	v_permlane32_swap_b32_e32 v208, v209
	v_mfma_f32_32x32x16_bf16 v[48:63], v[104:107], v[244:247], v[48:63]
	v_max_f32_e32 v233, v208, v209
	s_mov_b32 s2, 0x4138aa3b
	v_cmp_ge_f32_e32 vcc, s2, v233
	v_mfma_f32_32x32x16_bf16 v[48:63], v[100:103], v[190:193], v[48:63]
	s_cmp_eq_u64 vcc, exec
	s_cbranch_scc0 .LBB0_836
	v_mov_b32_e32 v233, 1.0
; #define SBAR() __builtin_amdgcn_sched_barrier(0)
; #define SLOAD(k0) do { vs0 = *reinterpret_cast<const bf16x8*>(&Vh[(size_t)((k0) + sr) * DM + sc]); vs1 = *reinterpret_cast<const bf16x8*>(&Vh[(size_t)((k0) + 32 + sr) * DM + sc]); \
;     ks = *reinterpret_cast<const bf16x8*>(&Kh[(size_t)((k0) + kr) * DM + kc]); } while (0)
; #define SWRITE(s) do { *(bf16x8*)(V_lds + (s) * SHM_V + vst0) = vs0; *(bf16x8*)(V_lds + (s) * SHM_V + vst1) = vs1; *(bf16x8*)(K_lds + (s) * SHM_K64 + kst) = ks; } while (0)
; #define RESC(a) do { if (__any((a) < 1.f)) { if (hi == 0) al_l[r32] = (a); asm volatile("s_waitcnt lgkmcnt(0)" ::: "memory"); \
;     _Pragma("unroll") for (int d = 0; d < 4; ++d) _Pragma("unroll") for (int r = 0; r < 16; ++r) o[d][r] *= al_l[crow(r, hi)]; } } while (0)
; #define ROT() do { s_prev = s_cur; s_cur = s_next; s_next = (s_next == DA_NBUF - 1) ? 0 : s_next + 1; } while (0)
; __device__ __forceinline__ void diff_pass(const bf16_t* __restrict__ Qb, const bf16_t* __restrict__ Kh, const bf16_t* __restrict__ Vh, int seq, char* lds, f32x16 (&o)[4], const int wave_) {
;     ...
;         YSEG(pB0, pB1, alB, s_prev);
;         SWRITE(s_next); RESC(alB); __syncthreads(); ROT();
;         SLOAD((j + 2) * 64);
;         SBAR(); qkt64c(pA0, pA1, K_lds + s_cur * SHM_K64, qr, negm, r32, hi); FIN(pB0, pB1, alB); SBAR();
.LBB0_825:
	ds_read_b64_tr_b16 v[190:191], v234 offset:0x600
	ds_read_b64_tr_b16 v[192:193], v234 offset:0xe00
	ds_read_b64_tr_b16 v[236:237], v234 offset:0x1600
	ds_read_b64_tr_b16 v[238:239], v234 offset:0x1e00
	ds_read_b64_tr_b16 v[240:241], v234 offset:0x2600
	ds_read_b64_tr_b16 v[242:243], v234 offset:0x2e00
	ds_read_b64_tr_b16 v[244:245], v234 offset:0x3600
	ds_read_b64_tr_b16 v[246:247], v234 offset:0x3e00
	s_waitcnt lgkmcnt(8)
	v_mfma_f32_32x32x16_bf16 v[32:47], v[96:99], v[124:127], v[32:47]
	v_exp_f32_e32 v128, v128
	v_exp_f32_e32 v129, v129
	v_exp_f32_e32 v130, v130
	v_mfma_f32_32x32x16_bf16 v[32:47], v[120:123], v[116:119], v[32:47]
	v_exp_f32_e32 v131, v131
	v_exp_f32_e32 v132, v132
	v_exp_f32_e32 v133, v133
	v_mfma_f32_32x32x16_bf16 v[32:47], v[104:107], v[112:115], v[32:47]
	v_exp_f32_e32 v134, v134
	v_exp_f32_e32 v135, v135
	v_exp_f32_e32 v136, v136
	v_mfma_f32_32x32x16_bf16 v[32:47], v[100:103], v[108:111], v[32:47]
	v_exp_f32_e32 v137, v137
	v_exp_f32_e32 v138, v138
	v_exp_f32_e32 v139, v139
	s_waitcnt lgkmcnt(0)
	s_lshl_b32 s2, s41, 14
	s_add_i32 s2, s2, 0
	s_lshl_b32 s3, s41, 13
	s_sub_i32 s2, s2, s3
	v_mfma_f32_32x32x16_bf16 v[16:31], v[96:99], v[190:193], v[16:31]
	v_exp_f32_e32 v140, v140
	v_exp_f32_e32 v141, v141
	v_exp_f32_e32 v142, v142
	v_mfma_f32_32x32x16_bf16 v[16:31], v[120:123], v[236:239], v[16:31]
	v_exp_f32_e32 v143, v143
	v_exp_f32_e32 v144, v144
	v_exp_f32_e32 v145, v145
	v_cmp_gt_f32_e32 vcc, 1.0, v233
	v_mfma_f32_32x32x16_bf16 v[16:31], v[104:107], v[240:243], v[16:31]
	v_exp_f32_e32 v146, v146
	v_exp_f32_e32 v147, v147
	v_exp_f32_e32 v148, v148
	v_mfma_f32_32x32x16_bf16 v[16:31], v[100:103], v[244:247], v[16:31]
	v_exp_f32_e32 v149, v149
	v_exp_f32_e32 v150, v150
	v_exp_f32_e32 v151, v151
	s_cbranch_vccz .LBB0_829
	s_and_saveexec_b64 s[12:13], s[0:1]
	ds_write_b32 v214, v233 offset:128
	s_or_b64 exec, exec, s[12:13]
	s_waitcnt lgkmcnt(0)
	v_add_u32_e32 v108, v213, v160
	ds_read_b128 v[96:99], v108 offset:224
	ds_read_b128 v[100:103], v108 offset:192
	ds_read_b128 v[104:107], v108 offset:160
	ds_read_b128 v[108:111], v108 offset:128
	s_waitcnt lgkmcnt(3)
	v_pk_mul_f32 v[12:13], v[12:13], v[96:97]
	s_waitcnt lgkmcnt(2)
	v_pk_mul_f32 v[8:9], v[8:9], v[100:101]
	s_waitcnt lgkmcnt(1)
	v_pk_mul_f32 v[4:5], v[4:5], v[104:105]
	v_pk_mul_f32 v[14:15], v[14:15], v[98:99]
	v_pk_mul_f32 v[10:11], v[10:11], v[102:103]
	v_pk_mul_f32 v[6:7], v[6:7], v[106:107]
	s_waitcnt lgkmcnt(0)
	v_pk_mul_f32 v[2:3], v[2:3], v[110:111]
	v_pk_mul_f32 v[0:1], v[0:1], v[108:109]
	v_pk_mul_f32 v[60:61], v[60:61], v[96:97]
	v_pk_mul_f32 v[56:57], v[56:57], v[100:101]
	v_pk_mul_f32 v[52:53], v[52:53], v[104:105]
	v_pk_mul_f32 v[62:63], v[62:63], v[98:99]
	v_pk_mul_f32 v[58:59], v[58:59], v[102:103]
	v_pk_mul_f32 v[54:55], v[54:55], v[106:107]
	v_pk_mul_f32 v[50:51], v[50:51], v[110:111]
	v_pk_mul_f32 v[48:49], v[48:49], v[108:109]
	v_pk_mul_f32 v[44:45], v[44:45], v[96:97]
	v_pk_mul_f32 v[40:41], v[40:41], v[100:101]
	v_pk_mul_f32 v[36:37], v[36:37], v[104:105]
	v_pk_mul_f32 v[46:47], v[46:47], v[98:99]
	v_pk_mul_f32 v[42:43], v[42:43], v[102:103]
	v_pk_mul_f32 v[38:39], v[38:39], v[106:107]
	v_pk_mul_f32 v[34:35], v[34:35], v[110:111]
	v_pk_mul_f32 v[32:33], v[32:33], v[108:109]
	v_pk_mul_f32 v[28:29], v[28:29], v[96:97]
	v_pk_mul_f32 v[24:25], v[24:25], v[100:101]
	v_pk_mul_f32 v[20:21], v[20:21], v[104:105]
	v_pk_mul_f32 v[30:31], v[30:31], v[98:99]
	v_pk_mul_f32 v[26:27], v[26:27], v[102:103]
	v_pk_mul_f32 v[22:23], v[22:23], v[106:107]
	v_pk_mul_f32 v[18:19], v[18:19], v[110:111]
	v_pk_mul_f32 v[16:17], v[16:17], v[108:109]
.LBB0_829:
	s_waitcnt lgkmcnt(0)
	v_add_u32_e32 v102, s2, v223
	v_add_u32_e32 v103, s2, v226
	v_add_u32_e32 v104, s2, v228
	v_add_u32_e32 v105, s2, v229
	s_waitcnt vmcnt(0)
	s_barrier
	ds_read_b128 v[112:115], v102 offset:49152
	ds_read_b128 v[116:119], v103 offset:49152
	ds_read_b128 v[120:123], v104 offset:49152
	ds_read_b128 v[124:127], v105 offset:49152
	ds_read_b128 v[190:193], v102 offset:53248
	ds_read_b128 v[202:205], v103 offset:53248
	ds_read_b128 v[234:237], v104 offset:53248
	ds_read_b128 v[238:241], v105 offset:53248
	s_add_i32 s3, s41, 1
	s_cmp_lg_u32 s41, 2
	s_cselect_b32 s3, s3, 0
	s_lshl_b32 s19, s3, 14
	s_add_i32 s19, s19, s18
	s_mov_b32 m0, s19
	s_lshl_b32 s20, s3, 13
	global_load_lds_dwordx4 v195, s[16:17]
	s_add_i32 m0, s19, 0x2000
	s_add_i32 s20, s20, s18
	global_load_lds_dwordx4 v255, s[16:17]
	s_add_i32 m0, s20, 0xc000
	s_add_u32 s16, s16, 0x20000
	global_load_lds_dwordx4 v194, s[14:15]
	s_addc_u32 s17, s17, 0
	s_add_u32 s14, s14, 0x20000
	s_addc_u32 s15, s15, 0
	v_exp_f32_e32 v208, v152
	v_exp_f32_e32 v209, v153
	v_add_f32_e32 v152, v128, v129
	v_add_f32_e32 v153, v130, v131
	s_waitcnt lgkmcnt(7)
	v_mfma_f32_32x32x16_bf16 v[96:111], v[112:115], v[162:165], v[80:95]
	v_exp_f32_e32 v210, v154
	v_add_f32_e32 v152, v152, v153
	v_add_f32_e32 v153, v132, v133
	v_add_f32_e32 v154, v134, v135
	v_exp_f32_e32 v211, v155
	s_waitcnt lgkmcnt(6)
	v_mfma_f32_32x32x16_bf16 v[96:111], v[116:119], v[166:169], v[96:111]
	v_add_f32_e32 v153, v153, v154
	v_add_f32_e32 v154, v136, v137
	v_add_f32_e32 v155, v138, v139
	v_add_f32_e32 v154, v154, v155
	v_add_f32_e32 v155, v140, v141
	s_waitcnt lgkmcnt(5)
	v_mfma_f32_32x32x16_bf16 v[96:111], v[120:123], v[170:173], v[96:111]
	v_exp_f32_e32 v156, v156
	v_exp_f32_e32 v157, v157
	v_exp_f32_e32 v158, v158
	v_exp_f32_e32 v159, v159
	s_waitcnt lgkmcnt(4)
	v_mfma_f32_32x32x16_bf16 v[96:111], v[124:127], v[174:177], v[96:111]
	s_waitcnt lgkmcnt(3)
; #define SBAR() __builtin_amdgcn_sched_barrier(0)
; __device__ __forceinline__ void diff_pass(const bf16_t* __restrict__ Qb, const bf16_t* __restrict__ Kh, const bf16_t* __restrict__ Vh, int seq, char* lds, f32x16 (&o)[4], const int wave_) {
;     ...
;         SBAR(); qkt64c(pA0, pA1, K_lds + s_cur * SHM_K64, qr, negm, r32, hi); FIN(pB0, pB1, alB); SBAR();
;         YSEG(pA0, pA1, alA, s_prev);
	v_mfma_f32_32x32x16_bf16 v[112:127], v[190:193], v[162:165], v[80:95]
	v_add_f32_e32 v190, v142, v143
	v_add_f32_e32 v155, v155, v190
	v_add_f32_e32 v190, v144, v145
	v_add_f32_e32 v191, v146, v147
	v_add_f32_e32 v190, v190, v191
	v_add_f32_e32 v152, v152, v190
	v_add_f32_e32 v190, v148, v149
	s_waitcnt lgkmcnt(2)
	v_mfma_f32_32x32x16_bf16 v[112:127], v[202:205], v[166:169], v[112:127]
	v_lshl_add_u32 v205, s42, 14, v217
	ds_read_b64_tr_b16 v[64:65], v205 offset:0
	ds_read_b64_tr_b16 v[66:67], v205 offset:0x800
	ds_read_b64_tr_b16 v[68:69], v205 offset:0x1000
	ds_read_b64_tr_b16 v[70:71], v205 offset:0x1800
	ds_read_b64_tr_b16 v[72:73], v205 offset:0x2000
	ds_read_b64_tr_b16 v[74:75], v205 offset:0x2800
	ds_read_b64_tr_b16 v[76:77], v205 offset:0x3000
	ds_read_b64_tr_b16 v[78:79], v205 offset:0x3800
	v_add_f32_e32 v191, v150, v151
	v_add_f32_e32 v190, v190, v191
	v_add_f32_e32 v153, v153, v190
	v_add_f32_e32 v190, v208, v209
	v_add_f32_e32 v191, v210, v211
	v_add_f32_e32 v190, v190, v191
	v_add_f32_e32 v154, v154, v190
	s_waitcnt lgkmcnt(9)
	v_mfma_f32_32x32x16_bf16 v[112:127], v[234:237], v[170:173], v[112:127]
	v_add_f32_e32 v190, v156, v157
	v_add_f32_e32 v191, v158, v159
	v_add_f32_e32 v190, v190, v191
	v_add_f32_e32 v155, v155, v190
	v_add_f32_e32 v152, v152, v153
	v_add_f32_e32 v153, v154, v155
	v_add_f32_e32 v203, v152, v153
	s_waitcnt lgkmcnt(8)
	v_mfma_f32_32x32x16_bf16 v[112:127], v[238:241], v[174:177], v[112:127]
	v_mov_b32_e32 v204, v203
	v_cvt_pk_bf16_f32 v152, v128, v129
	v_cvt_pk_bf16_f32 v153, v130, v131
	v_cvt_pk_bf16_f32 v154, v132, v133
	v_cvt_pk_bf16_f32 v155, v134, v135
	v_cvt_pk_bf16_f32 v136, v136, v137
	v_cvt_pk_bf16_f32 v137, v138, v139
	v_cvt_pk_bf16_f32 v138, v140, v141
	v_cvt_pk_bf16_f32 v139, v142, v143
	v_permlane32_swap_b32_e32 v152, v154
	v_permlane32_swap_b32_e32 v153, v155
	v_cvt_pk_bf16_f32 v132, v144, v145
	v_cvt_pk_bf16_f32 v133, v146, v147
	v_cvt_pk_bf16_f32 v134, v148, v149
	v_cvt_pk_bf16_f32 v135, v150, v151
	s_waitcnt lgkmcnt(0)
	v_mfma_f32_32x32x16_bf16 v[0:15], v[152:155], v[64:67], v[0:15]
	v_permlane32_swap_b32_e32 v136, v138
	v_permlane32_swap_b32_e32 v137, v139
	v_cvt_pk_bf16_f32 v128, v208, v209
	v_cvt_pk_bf16_f32 v129, v210, v211
	v_cvt_pk_bf16_f32 v130, v156, v157
	v_cvt_pk_bf16_f32 v131, v158, v159
	v_mfma_f32_32x32x16_bf16 v[0:15], v[136:139], v[68:71], v[0:15]
	v_permlane32_swap_b32_e32 v132, v134
	v_permlane32_swap_b32_e32 v133, v135
	ds_read_b64_tr_b16 v[190:191], v205 offset:0x200
	ds_read_b64_tr_b16 v[192:193], v205 offset:0xa00
	ds_read_b64_tr_b16 v[234:235], v205 offset:0x1200
	ds_read_b64_tr_b16 v[236:237], v205 offset:0x1a00
	ds_read_b64_tr_b16 v[238:239], v205 offset:0x2200
	ds_read_b64_tr_b16 v[240:241], v205 offset:0x2a00
	ds_read_b64_tr_b16 v[242:243], v205 offset:0x3200
	ds_read_b64_tr_b16 v[244:245], v205 offset:0x3a00
	v_mfma_f32_32x32x16_bf16 v[0:15], v[132:135], v[72:75], v[0:15]
	v_permlane32_swap_b32_e32 v128, v130
	v_permlane32_swap_b32_e32 v129, v131
	v_permlane32_swap_b32_e32 v203, v204
	v_max_f32_e32 v140, v96, v97
	v_max3_f32 v140, v140, v112, v114
	v_max3_f32 v141, v98, v99, v113
	v_max3_f32 v140, v140, v115, v100
	v_max3_f32 v141, v141, v102, v103
	v_mfma_f32_32x32x16_bf16 v[0:15], v[128:131], v[76:79], v[0:15]
	v_max3_f32 v202, v140, v101, v116
	v_max3_f32 v208, v141, v118, v119
	ds_read_b64_tr_b16 v[156:157], v205 offset:0x400
	ds_read_b64_tr_b16 v[158:159], v205 offset:0xc00
	ds_read_b64_tr_b16 v[148:149], v205 offset:0x1400
	ds_read_b64_tr_b16 v[150:151], v205 offset:0x1c00
	ds_read_b64_tr_b16 v[144:145], v205 offset:0x2400
	ds_read_b64_tr_b16 v[146:147], v205 offset:0x2c00
	ds_read_b64_tr_b16 v[140:141], v205 offset:0x3400
	ds_read_b64_tr_b16 v[142:143], v205 offset:0x3c00
	s_waitcnt lgkmcnt(8)
	v_mfma_f32_32x32x16_bf16 v[48:63], v[152:155], v[190:193], v[48:63]
	v_max3_f32 v190, v202, v117, v104
	v_max3_f32 v191, v208, v106, v107
	v_max3_f32 v190, v190, v105, v120
	v_max3_f32 v191, v191, v122, v123
	v_max3_f32 v190, v190, v121, v108
	v_max3_f32 v191, v191, v110, v111
	v_max3_f32 v190, v190, v109, v124
	v_mfma_f32_32x32x16_bf16 v[48:63], v[136:139], v[234:237], v[48:63]
	v_max3_f32 v191, v191, v126, v127
	v_max3_f32 v190, v190, v125, v191
	v_mov_b32_e32 v191, v190
	s_nop 1
	v_permlane32_swap_b32_e32 v190, v191
	v_mfma_f32_32x32x16_bf16 v[48:63], v[132:135], v[238:241], v[48:63]
	v_max_f32_e32 v234, v190, v191
	s_mov_b32 s2, 0x4138aa3b
	v_cmp_ge_f32_e32 vcc, s2, v234
	v_mfma_f32_32x32x16_bf16 v[48:63], v[128:131], v[242:245], v[48:63]
	s_cmp_eq_u64 vcc, exec
	v_mov_b32_e32 v202, 1.0
	s_cbranch_scc0 .LBB0_837
.LBB0_830:
	ds_read_b64_tr_b16 v[190:191], v205 offset:0x600
	ds_read_b64_tr_b16 v[192:193], v205 offset:0xe00
	ds_read_b64_tr_b16 v[234:235], v205 offset:0x1600
	ds_read_b64_tr_b16 v[236:237], v205 offset:0x1e00
	ds_read_b64_tr_b16 v[238:239], v205 offset:0x2600
	ds_read_b64_tr_b16 v[240:241], v205 offset:0x2e00
	ds_read_b64_tr_b16 v[242:243], v205 offset:0x3600
	ds_read_b64_tr_b16 v[244:245], v205 offset:0x3e00
	s_add_i32 s2, s41, 1
	s_waitcnt lgkmcnt(8)
	s_cmp_lg_u32 s41, 2
	s_cselect_b32 s42, s2, 0
	v_mfma_f32_32x32x16_bf16 v[32:47], v[152:155], v[156:159], v[32:47]
	v_exp_f32_e32 v96, v96
	v_exp_f32_e32 v97, v97
	v_exp_f32_e32 v98, v98
	v_mfma_f32_32x32x16_bf16 v[32:47], v[136:139], v[148:151], v[32:47]
	v_exp_f32_e32 v99, v99
	v_exp_f32_e32 v100, v100
	v_exp_f32_e32 v101, v101
	v_mfma_f32_32x32x16_bf16 v[32:47], v[132:135], v[144:147], v[32:47]
	v_exp_f32_e32 v102, v102
	v_exp_f32_e32 v103, v103
	v_exp_f32_e32 v104, v104
	v_mfma_f32_32x32x16_bf16 v[32:47], v[128:131], v[140:143], v[32:47]
	v_exp_f32_e32 v105, v105
	v_exp_f32_e32 v106, v106
	v_exp_f32_e32 v107, v107
	s_waitcnt lgkmcnt(0)
	s_lshl_b32 s2, s42, 14
	s_add_i32 s2, s2, 0
	v_mfma_f32_32x32x16_bf16 v[16:31], v[152:155], v[190:193], v[16:31]
	v_exp_f32_e32 v108, v108
	v_exp_f32_e32 v109, v109
	v_exp_f32_e32 v110, v110
	v_mfma_f32_32x32x16_bf16 v[16:31], v[136:139], v[234:237], v[16:31]
	v_exp_f32_e32 v111, v111
	v_exp_f32_e32 v112, v112
	v_exp_f32_e32 v113, v113
	v_cmp_gt_f32_e32 vcc, 1.0, v202
	v_mfma_f32_32x32x16_bf16 v[16:31], v[132:135], v[238:241], v[16:31]
	v_exp_f32_e32 v114, v114
	v_exp_f32_e32 v115, v115
	v_exp_f32_e32 v116, v116
	v_mfma_f32_32x32x16_bf16 v[16:31], v[128:131], v[242:245], v[16:31]
	v_exp_f32_e32 v117, v117
	v_exp_f32_e32 v118, v118
	v_exp_f32_e32 v119, v119
	s_cbranch_vccz .LBB0_834
	s_and_saveexec_b64 s[12:13], s[0:1]
	ds_write_b32 v214, v202 offset:128
	s_or_b64 exec, exec, s[12:13]
	s_waitcnt lgkmcnt(0)
	v_add_u32_e32 v140, v213, v160
	ds_read_b128 v[128:131], v140 offset:224
	ds_read_b128 v[132:135], v140 offset:192
	ds_read_b128 v[136:139], v140 offset:160
	ds_read_b128 v[140:143], v140 offset:128
	s_waitcnt lgkmcnt(3)
	v_pk_mul_f32 v[12:13], v[12:13], v[128:129]
	s_waitcnt lgkmcnt(2)
	v_pk_mul_f32 v[8:9], v[8:9], v[132:133]
	s_waitcnt lgkmcnt(1)
	v_pk_mul_f32 v[4:5], v[4:5], v[136:137]
	v_pk_mul_f32 v[14:15], v[14:15], v[130:131]
	v_pk_mul_f32 v[10:11], v[10:11], v[134:135]
	v_pk_mul_f32 v[6:7], v[6:7], v[138:139]
	s_waitcnt lgkmcnt(0)
	v_pk_mul_f32 v[2:3], v[2:3], v[142:143]
	v_pk_mul_f32 v[0:1], v[0:1], v[140:141]
	v_pk_mul_f32 v[60:61], v[60:61], v[128:129]
	v_pk_mul_f32 v[56:57], v[56:57], v[132:133]
	v_pk_mul_f32 v[52:53], v[52:53], v[136:137]
	v_pk_mul_f32 v[62:63], v[62:63], v[130:131]
	v_pk_mul_f32 v[58:59], v[58:59], v[134:135]
	v_pk_mul_f32 v[54:55], v[54:55], v[138:139]
	v_pk_mul_f32 v[50:51], v[50:51], v[142:143]
	v_pk_mul_f32 v[48:49], v[48:49], v[140:141]
	v_pk_mul_f32 v[44:45], v[44:45], v[128:129]
	v_pk_mul_f32 v[40:41], v[40:41], v[132:133]
	v_pk_mul_f32 v[36:37], v[36:37], v[136:137]
	v_pk_mul_f32 v[46:47], v[46:47], v[130:131]
	v_pk_mul_f32 v[42:43], v[42:43], v[134:135]
	v_pk_mul_f32 v[38:39], v[38:39], v[138:139]
	v_pk_mul_f32 v[34:35], v[34:35], v[142:143]
	v_pk_mul_f32 v[32:33], v[32:33], v[140:141]
	v_pk_mul_f32 v[28:29], v[28:29], v[128:129]
	v_pk_mul_f32 v[24:25], v[24:25], v[132:133]
	v_pk_mul_f32 v[20:21], v[20:21], v[136:137]
	v_pk_mul_f32 v[30:31], v[30:31], v[130:131]
	v_pk_mul_f32 v[26:27], v[26:27], v[134:135]
	v_pk_mul_f32 v[22:23], v[22:23], v[138:139]
	v_pk_mul_f32 v[18:19], v[18:19], v[142:143]
	v_pk_mul_f32 v[16:17], v[16:17], v[140:141]
.LBB0_834:
	s_add_i32 s2, s42, 1
	v_add_f32_e32 v128, v231, v232
	s_cmp_lg_u32 s42, 2
	v_fmac_f32_e32 v128, v215, v230
	v_add_f32_e32 v215, v203, v204
	s_cselect_b32 s2, s2, 0
	s_add_i32 s40, s40, 2
	v_fmac_f32_e32 v215, v128, v233
	s_lshl_b32 s3, s42, 13
	s_cmp_gt_u32 s40, 28
	v_add_u32_e32 v128, s3, v223
	v_add_u32_e32 v129, s3, v226
	v_add_u32_e32 v130, s3, v228
	v_add_u32_e32 v131, s3, v229
	v_mov_b32_e32 v230, v202
	s_mov_b32 s12, s41
	s_mov_b32 s41, s2
	s_waitcnt lgkmcnt(0)
	s_waitcnt vmcnt(0)
	s_barrier
	s_cbranch_scc1 .LBB0_838
	s_branch .Latt9_p1_top

; #define SBAR() __builtin_amdgcn_sched_barrier(0)
; __device__ __forceinline__ int crow(int r, int hi) { return (r & 3) + 8 * (r >> 2) + 4 * hi; }
; #define RESC(a) do { if (__any((a) < 1.f)) { if (hi == 0) al_l[r32] = (a); asm volatile("s_waitcnt lgkmcnt(0)" ::: "memory"); \
;     _Pragma("unroll") for (int d = 0; d < 4; ++d) _Pragma("unroll") for (int r = 0; r < 16; ++r) o[d][r] *= al_l[crow(r, hi)]; } } while (0)
; template <int D0> __device__ __forceinline__ void pv_one(f32x16& od, int vb, bf16x8 pa0, bf16x8 pa1, bf16x8 pa2, bf16x8 pa3) {
;     const s16x4 l0 = tr_read<v_rd_off(D0, 0, 0)>(vb), h0 = tr_read<v_rd_off(D0, 0, 1)>(vb), l1 = tr_read<v_rd_off(D0, 1, 0)>(vb), h1 = tr_read<v_rd_off(D0, 1, 1)>(vb);
;     const s16x4 l2 = tr_read<v_rd_off(D0, 2, 0)>(vb), h2 = tr_read<v_rd_off(D0, 2, 1)>(vb), l3 = tr_read<v_rd_off(D0, 3, 0)>(vb), h3 = tr_read<v_rd_off(D0, 3, 1)>(vb);
;     asm volatile("s_waitcnt lgkmcnt(0)" ::: "memory"); SBAR();
;     ...
;     od = __builtin_amdgcn_mfma_f32_32x32x16_bf16(pa0, PK(l0, h0), od, 0, 0, 0);
;     od = __builtin_amdgcn_mfma_f32_32x32x16_bf16(pa1, PK(l1, h1), od, 0, 0, 0);
;     od = __builtin_amdgcn_mfma_f32_32x32x16_bf16(pa2, PK(l2, h2), od, 0, 0, 0);
;     od = __builtin_amdgcn_mfma_f32_32x32x16_bf16(pa3, PK(l3, h3), od, 0, 0, 0);
;     ...
; }
; __device__ __forceinline__ void pv_d0(f32x16* o, int vb, bf16x8 pa0, bf16x8 pa1, bf16x8 pa2, bf16x8 pa3) {
;     pv_one<0>(o[0], vb, pa0, pa1, pa2, pa3); pv_one<1>(o[1], vb, pa0, pa1, pa2, pa3); pv_one<2>(o[2], vb, pa0, pa1, pa2, pa3); pv_one<3>(o[3], vb, pa0, pa1, pa2, pa3);
; __device__ __forceinline__ void diff_pass(const bf16_t* __restrict__ Qb, const bf16_t* __restrict__ Kh, const bf16_t* __restrict__ Vh, int seq, char* lds, f32x16 (&o)[4], const int wave_) {
;     ...
;     SBAR(); qkt64c(pB0, pB1, K_lds + s_cur * SHM_K64, qr, negm, r32, hi); FIN(pA0, pA1, alA); SBAR();
;     YSEG(pB0, pB1, alB, s_prev);
;     RESC(alB);
;     FIN(pB0, pB1, alB); SBAR();
;     pv_d0(o, vb0 + s_cur * SHM_V, pa0, pa1, pa2, pa3);
;     if (hi == 0) li_l[r32] = l_reg; asm volatile("s_waitcnt lgkmcnt(0)" ::: "memory");
; #pragma unroll
;     for (int r = 0; r < 16; ++r) { const float rl = __builtin_amdgcn_rcpf(li_l[crow(r, hi)]);
; #pragma unroll
;         for (int d = 0; d < 4; ++d) o[d][r] *= rl; }
.LBB0_843:
	v_exp_f32_e32 v96, v72
	v_exp_f32_e32 v97, v73
	v_add_f32_e32 v72, v80, v81
	v_add_f32_e32 v73, v82, v83
	v_exp_f32_e32 v98, v74
	v_add_f32_e32 v72, v72, v73
	v_add_f32_e32 v73, v84, v85
	v_add_f32_e32 v74, v86, v87
	v_exp_f32_e32 v99, v75
	v_add_f32_e32 v73, v73, v74
	v_add_f32_e32 v74, v88, v89
	v_add_f32_e32 v75, v90, v91
	v_exp_f32_e32 v100, v76
	v_add_f32_e32 v74, v74, v75
	v_add_f32_e32 v75, v92, v93
	v_add_f32_e32 v76, v94, v95
	v_exp_f32_e32 v101, v77
	v_add_f32_e32 v75, v75, v76
	v_add_f32_e32 v76, v64, v65
	v_add_f32_e32 v77, v66, v67
	v_add_f32_e32 v76, v76, v77
	v_exp_f32_e32 v102, v78
	v_exp_f32_e32 v103, v79
	v_add_f32_e32 v72, v72, v76
	v_add_f32_e32 v76, v68, v69
	v_add_f32_e32 v77, v70, v71
	v_add_f32_e32 v76, v76, v77
	v_add_f32_e32 v73, v73, v76
	v_add_f32_e32 v76, v96, v97
	v_add_f32_e32 v77, v98, v99
	v_add_f32_e32 v76, v76, v77
	v_add_f32_e32 v74, v74, v76
	v_add_f32_e32 v76, v100, v101
	v_add_f32_e32 v77, v102, v103
	v_add_f32_e32 v76, v76, v77
	v_add_f32_e32 v75, v75, v76
	v_add_f32_e32 v72, v72, v73
	v_add_f32_e32 v73, v74, v75
	v_add_f32_e32 v72, v72, v73
	v_mov_b32_e32 v73, v72
	s_nop 1
	v_permlane32_swap_b32_e32 v72, v73
	v_cvt_pk_bf16_f32 v74, v80, v81
	v_cvt_pk_bf16_f32 v75, v82, v83
	v_cvt_pk_bf16_f32 v76, v84, v85
	v_cvt_pk_bf16_f32 v77, v86, v87
	v_cvt_pk_bf16_f32 v78, v88, v89
	v_cvt_pk_bf16_f32 v79, v90, v91
	v_cvt_pk_bf16_f32 v80, v92, v93
	v_cvt_pk_bf16_f32 v81, v94, v95
	v_cvt_pk_bf16_f32 v64, v64, v65
	v_cvt_pk_bf16_f32 v65, v66, v67
	v_cvt_pk_bf16_f32 v66, v68, v69
	v_cvt_pk_bf16_f32 v67, v70, v71
	v_cvt_pk_bf16_f32 v68, v96, v97
	v_cvt_pk_bf16_f32 v69, v98, v99
	v_cvt_pk_bf16_f32 v70, v100, v101
	v_cvt_pk_bf16_f32 v71, v102, v103
	s_nop 0
	v_permlane32_swap_b32_e32 v74, v76
	v_permlane32_swap_b32_e32 v75, v77
	v_permlane32_swap_b32_e32 v78, v80
	v_permlane32_swap_b32_e32 v79, v81
	v_permlane32_swap_b32_e32 v64, v66
	v_permlane32_swap_b32_e32 v65, v67
	v_permlane32_swap_b32_e32 v68, v70
	v_permlane32_swap_b32_e32 v69, v71
	s_cmp_lg_u32 0, -1
	s_cselect_b32 s2, 0, 0
	s_addk_i32 s2, 0x4000
	v_add_u32_e32 v98, s2, v216
	ds_read_b64_tr_b16 v[82:83], v98 offset:0
	ds_read_b64_tr_b16 v[84:85], v98 offset:0x800
	ds_read_b64_tr_b16 v[86:87], v98 offset:0x1000
	ds_read_b64_tr_b16 v[88:89], v98 offset:0x1800
	ds_read_b64_tr_b16 v[90:91], v98 offset:0x2000
	ds_read_b64_tr_b16 v[92:93], v98 offset:0x2800
	ds_read_b64_tr_b16 v[94:95], v98 offset:0x3000
	ds_read_b64_tr_b16 v[96:97], v98 offset:0x3800
	s_waitcnt lgkmcnt(0)
	s_nop 0
	v_mfma_f32_32x32x16_bf16 v[0:15], v[74:77], v[82:85], v[0:15]
	ds_read_b64_tr_b16 v[82:83], v98 offset:0x200
	ds_read_b64_tr_b16 v[84:85], v98 offset:0xa00
	v_mfma_f32_32x32x16_bf16 v[0:15], v[78:81], v[86:89], v[0:15]
	ds_read_b64_tr_b16 v[86:87], v98 offset:0x1200
	ds_read_b64_tr_b16 v[88:89], v98 offset:0x1a00
	v_mfma_f32_32x32x16_bf16 v[0:15], v[64:67], v[90:93], v[0:15]
	ds_read_b64_tr_b16 v[90:91], v98 offset:0x2200
	ds_read_b64_tr_b16 v[92:93], v98 offset:0x2a00
	v_mfma_f32_32x32x16_bf16 v[0:15], v[68:71], v[94:97], v[0:15]
	ds_read_b64_tr_b16 v[94:95], v98 offset:0x3200
	ds_read_b64_tr_b16 v[96:97], v98 offset:0x3a00
	s_waitcnt lgkmcnt(0)
	v_mfma_f32_32x32x16_bf16 v[48:63], v[74:77], v[82:85], v[48:63]
	ds_read_b64_tr_b16 v[82:83], v98 offset:0x400
	ds_read_b64_tr_b16 v[84:85], v98 offset:0xc00
	v_mfma_f32_32x32x16_bf16 v[48:63], v[78:81], v[86:89], v[48:63]
	ds_read_b64_tr_b16 v[86:87], v98 offset:0x1400
	ds_read_b64_tr_b16 v[88:89], v98 offset:0x1c00
	v_mfma_f32_32x32x16_bf16 v[48:63], v[64:67], v[90:93], v[48:63]
	ds_read_b64_tr_b16 v[90:91], v98 offset:0x2400
	ds_read_b64_tr_b16 v[92:93], v98 offset:0x2c00
	v_mfma_f32_32x32x16_bf16 v[48:63], v[68:71], v[94:97], v[48:63]
	ds_read_b64_tr_b16 v[94:95], v98 offset:0x3400
	ds_read_b64_tr_b16 v[96:97], v98 offset:0x3c00
	s_waitcnt lgkmcnt(0)
	v_mfma_f32_32x32x16_bf16 v[32:47], v[74:77], v[82:85], v[32:47]
	ds_read_b64_tr_b16 v[82:83], v98 offset:0x600
	ds_read_b64_tr_b16 v[84:85], v98 offset:0xe00
	v_mfma_f32_32x32x16_bf16 v[32:47], v[78:81], v[86:89], v[32:47]
	ds_read_b64_tr_b16 v[86:87], v98 offset:0x1600
	ds_read_b64_tr_b16 v[88:89], v98 offset:0x1e00
	v_mfma_f32_32x32x16_bf16 v[32:47], v[64:67], v[90:93], v[32:47]
	ds_read_b64_tr_b16 v[90:91], v98 offset:0x2600
	ds_read_b64_tr_b16 v[92:93], v98 offset:0x2e00
	v_mfma_f32_32x32x16_bf16 v[32:47], v[68:71], v[94:97], v[32:47]
	ds_read_b64_tr_b16 v[94:95], v98 offset:0x3600
	ds_read_b64_tr_b16 v[96:97], v98 offset:0x3e00
	s_waitcnt lgkmcnt(0)
	v_mfma_f32_32x32x16_bf16 v[16:31], v[74:77], v[82:85], v[16:31]
	v_mfma_f32_32x32x16_bf16 v[16:31], v[78:81], v[86:89], v[16:31]
	v_mfma_f32_32x32x16_bf16 v[16:31], v[64:67], v[90:93], v[16:31]
	v_mfma_f32_32x32x16_bf16 v[16:31], v[68:71], v[94:97], v[16:31]
	s_and_saveexec_b64 s[12:13], s[0:1]
	v_add_f32_e32 v64, v128, v129
	v_fmac_f32_e32 v64, v215, v202
	v_add_f32_e32 v65, v72, v73
	v_fmac_f32_e32 v65, v64, v130
	ds_write_b32 v214, v65
	s_or_b64 exec, exec, s[12:13]
	s_waitcnt lgkmcnt(0)
	v_add_u32_e32 v72, v213, v160
	ds_read_b128 v[64:67], v72
	ds_read_b128 v[68:71], v72 offset:32
	v_ashrrev_i32_e32 v214, 6, v207
	s_add_i32 s0, 0, 0x12800
	v_and_b32_e32 v213, 63, v207
	s_waitcnt lgkmcnt(1)
	v_rcp_f32_e32 v64, v64
	v_rcp_f32_e32 v65, v65
	v_lshl_add_u32 v215, v214, 13, s0
	v_lshl_add_u32 v216, v213, 2, v215
	v_mul_f32_e32 v73, v0, v64
	v_rcp_f32_e32 v0, v66
	v_mul_f32_e32 v48, v48, v64
	v_mul_f32_e32 v32, v32, v64
	v_mul_f32_e32 v16, v16, v64
	v_mul_f32_e32 v64, v1, v65
	v_mul_f32_e32 v49, v49, v65
	v_mul_f32_e32 v33, v33, v65
	v_mul_f32_e32 v17, v17, v65
	v_mul_f32_e32 v65, v2, v0
	v_rcp_f32_e32 v1, v67
	v_mul_f32_e32 v50, v50, v0
	v_mul_f32_e32 v34, v34, v0
	v_mul_f32_e32 v18, v18, v0
	s_waitcnt lgkmcnt(0)
; __device__ __forceinline__ unsigned cvt_pk_bf16(float lo, float hi) { unsigned r; asm volatile("v_cvt_pk_bf16_f32 %0, %1, %2" : "=v"(r) : "v"(lo), "v"(hi)); return r; }
; __device__ __forceinline__ int fresh_lane() { unsigned m = ~0u; asm volatile("" : "+s"(m)); return (int)__builtin_amdgcn_mbcnt_hi(m, __builtin_amdgcn_mbcnt_lo(m, 0u)); }
; __device__ __forceinline__ int crow(int r, int hi) { return (r & 3) + 8 * (r >> 2) + 4 * hi; }
; __device__ __forceinline__ void diff_pass(const bf16_t* __restrict__ Qb, const bf16_t* __restrict__ Kh, const bf16_t* __restrict__ Vh, int seq, char* lds, f32x16 (&o)[4], const int wave_) {
;     ...
; #pragma unroll
;     for (int r = 0; r < 16; ++r) { const float rl = __builtin_amdgcn_rcpf(li_l[crow(r, hi)]);
; #pragma unroll
;         for (int d = 0; d < 4; ++d) o[d][r] *= rl; }
;     ...
; }
; __device__ __forceinline__ void diff_unit(int b, int h, int qb, const bf16_t* Q, const bf16_t* K, const bf16_t* V, bf16_t* YA, float lam, float omli, const float* subln, char* lds, const int wave_) {
;     int tid_ = (wave_ << 6) | fresh_lane(); asm volatile("" : "+v"(tid_));
;     const int tid = tid_, wid = tid >> 6, lane = tid & 63, r32 = lane & 31, hi = lane >> 5;
;     const size_t rowbase = (size_t)b * SEQ; const int q0 = qb * 256;
;     const bf16_t* Qb = Q + (rowbase + q0) * DM + h * 128;
;     const bf16_t* Kh = K + rowbase * DM + h * 128;
;     const bf16_t* Vh = V + rowbase * DM + h * 128;
;     f32x16 o[4];
;     diff_pass(Qb, Kh, Vh, SEQ, lds, o, wave_);
;     unsigned* park = (unsigned*)(lds + DA_LDS) + wid * 2048 + lane;
; #pragma unroll
;     for (int d = 0; d < 4; ++d)
; #pragma unroll
;         for (int r = 0; r < 8; ++r) park[(d * 8 + r) * 64] = cvt_pk_bf16(o[d][2 * r], o[d][2 * r + 1]);
;     diff_pass(Qb + 64, Kh + 64, Vh, SEQ, lds, o, wave_);
	v_rcp_f32_e32 v0, v68
	v_mul_f32_e32 v66, v3, v1
	v_mul_f32_e32 v51, v51, v1
	v_mul_f32_e32 v35, v35, v1
	v_mul_f32_e32 v19, v19, v1
	v_mul_f32_e32 v67, v4, v0
	v_rcp_f32_e32 v1, v69
	v_rcp_f32_e32 v4, v70
	v_rcp_f32_e32 v70, v71
	v_mul_f32_e32 v52, v52, v0
	v_mul_f32_e32 v36, v36, v0
	v_mul_f32_e32 v20, v20, v0
	v_mul_f32_e32 v68, v5, v1
	v_mul_f32_e32 v53, v53, v1
	v_mul_f32_e32 v37, v37, v1
	v_mul_f32_e32 v21, v21, v1
	v_mul_f32_e32 v69, v6, v4
	v_mul_f32_e32 v54, v54, v4
	ds_read_b128 v[0:3], v72 offset:64
	v_mul_f32_e32 v38, v38, v4
	v_mul_f32_e32 v22, v22, v4
	v_mul_f32_e32 v71, v7, v70
	ds_read_b128 v[4:7], v72 offset:96
	s_waitcnt lgkmcnt(1)
	v_rcp_f32_e32 v0, v0
	v_rcp_f32_e32 v1, v1
	v_rcp_f32_e32 v2, v2
	v_rcp_f32_e32 v3, v3
	s_waitcnt lgkmcnt(0)
	v_rcp_f32_e32 v4, v4
	v_rcp_f32_e32 v5, v5
	v_rcp_f32_e32 v6, v6
	v_rcp_f32_e32 v7, v7
	v_mul_f32_e32 v8, v8, v0
	v_mul_f32_e32 v56, v56, v0
	v_mul_f32_e32 v40, v40, v0
	v_mul_f32_e32 v0, v24, v0
	v_mul_f32_e32 v9, v9, v1
	v_mul_f32_e32 v24, v57, v1
	v_mul_f32_e32 v41, v41, v1
	v_mul_f32_e32 v1, v25, v1
	v_mul_f32_e32 v10, v10, v2
	v_mul_f32_e32 v25, v58, v2
	v_mul_f32_e32 v42, v42, v2
	v_mul_f32_e32 v2, v26, v2
	v_mul_f32_e32 v11, v11, v3
	v_mul_f32_e32 v26, v59, v3
	v_mul_f32_e32 v43, v43, v3
	v_mul_f32_e32 v3, v27, v3
	v_mul_f32_e32 v12, v12, v4
	v_mul_f32_e32 v27, v60, v4
	v_mul_f32_e32 v44, v44, v4
	v_mul_f32_e32 v4, v28, v4
	v_mul_f32_e32 v13, v13, v5
	v_mul_f32_e32 v28, v61, v5
	v_mul_f32_e32 v45, v45, v5
	v_mul_f32_e32 v5, v29, v5
	v_mul_f32_e32 v14, v14, v6
	v_mul_f32_e32 v29, v62, v6
	v_mul_f32_e32 v46, v46, v6
	v_mul_f32_e32 v6, v30, v6
	v_mul_f32_e32 v15, v15, v7
	v_mul_f32_e32 v30, v63, v7
	v_mul_f32_e32 v47, v47, v7
	v_mul_f32_e32 v7, v31, v7
	v_cvt_pk_bf16_f32 v31, v73, v64
	ds_write_b32 v216, v31
	v_cvt_pk_bf16_f32 v31, v65, v66
	ds_write_b32 v216, v31 offset:256
	v_cvt_pk_bf16_f32 v31, v67, v68
	ds_write_b32 v216, v31 offset:512
	v_cvt_pk_bf16_f32 v31, v69, v71
	ds_write_b32 v216, v31 offset:768
	v_cvt_pk_bf16_f32 v8, v8, v9
	ds_write_b32 v216, v8 offset:1024
	v_cvt_pk_bf16_f32 v8, v10, v11
	ds_write_b32 v216, v8 offset:1280
	v_cvt_pk_bf16_f32 v8, v12, v13
	ds_write_b32 v216, v8 offset:1536
	v_cvt_pk_bf16_f32 v8, v14, v15
	ds_write_b32 v216, v8 offset:1792
	v_cvt_pk_bf16_f32 v8, v48, v49
	ds_write_b32 v216, v8 offset:2048
	v_cvt_pk_bf16_f32 v8, v50, v51
	ds_write_b32 v216, v8 offset:2304
	v_cvt_pk_bf16_f32 v8, v52, v53
	v_mul_f32_e32 v55, v55, v70
	ds_write_b32 v216, v8 offset:2560
	v_cvt_pk_bf16_f32 v8, v54, v55
	ds_write_b32 v216, v8 offset:2816
	v_cvt_pk_bf16_f32 v8, v56, v24
	ds_write_b32 v216, v8 offset:3072
	v_cvt_pk_bf16_f32 v8, v25, v26
	ds_write_b32 v216, v8 offset:3328
	v_cvt_pk_bf16_f32 v8, v27, v28
	ds_write_b32 v216, v8 offset:3584
	v_cvt_pk_bf16_f32 v8, v29, v30
	ds_write_b32 v216, v8 offset:3840
	v_cvt_pk_bf16_f32 v8, v32, v33
	ds_write_b32 v216, v8 offset:4096
	v_cvt_pk_bf16_f32 v8, v34, v35
	ds_write_b32 v216, v8 offset:4352
	v_cvt_pk_bf16_f32 v8, v36, v37
	v_mul_f32_e32 v39, v39, v70
	ds_write_b32 v216, v8 offset:4608
	v_cvt_pk_bf16_f32 v8, v38, v39
	ds_write_b32 v216, v8 offset:4864
	v_cvt_pk_bf16_f32 v8, v40, v41
	ds_write_b32 v216, v8 offset:5120
	v_cvt_pk_bf16_f32 v8, v42, v43
	ds_write_b32 v216, v8 offset:5376
	v_cvt_pk_bf16_f32 v8, v44, v45
	ds_write_b32 v216, v8 offset:5632
	v_cvt_pk_bf16_f32 v8, v46, v47
	ds_write_b32 v216, v8 offset:5888
	v_cvt_pk_bf16_f32 v8, v16, v17
	ds_write_b32 v216, v8 offset:6144
	v_cvt_pk_bf16_f32 v8, v18, v19
	ds_write_b32 v216, v8 offset:6400
	v_cvt_pk_bf16_f32 v8, v20, v21
	v_mul_f32_e32 v23, v23, v70
	ds_write_b32 v216, v8 offset:6656
	v_cvt_pk_bf16_f32 v8, v22, v23
	ds_write_b32 v216, v8 offset:6912
	v_cvt_pk_bf16_f32 v0, v0, v1
	ds_write_b32 v216, v0 offset:7168
	v_cvt_pk_bf16_f32 v0, v2, v3
	ds_write_b32 v216, v0 offset:7424
	v_cvt_pk_bf16_f32 v0, v4, v5
	ds_write_b32 v216, v0 offset:7680
	v_cvt_pk_bf16_f32 v0, v6, v7
	s_mov_b32 s0, -1
	ds_write_b32 v216, v0 offset:7936
	v_mov_b32_e32 v5, v161
	v_mbcnt_lo_u32_b32 v0, s0, 0
	v_mbcnt_hi_u32_b32 v0, s0, v0
	v_or_b32_e32 v68, s55, v0
	s_movk_i32 s0, 0xffe0
	v_ashrrev_i32_e32 v0, 1, v68
	v_bfi_b32 v0, s0, v0, v68
	v_ashrrev_i32_e32 v1, 31, v0
	v_lshlrev_b64 v[0:1], 11, v[0:1]
	v_lshrrev_b32_e32 v2, 1, v68
	v_ashrrev_i32_e32 v12, 4, v68
	v_lshl_add_u64 v[0:1], s[34:35], 0, v[0:1]
	v_and_b32_e32 v160, 16, v2
	v_lshlrev_b32_e32 v24, 3, v68
	v_ashrrev_i32_e32 v13, 31, v12
	v_lshl_add_u64 v[0:1], v[0:1], 0, v[160:161]
	v_and_b32_e32 v2, 0x78, v24
	v_lshlrev_b64 v[48:49], 11, v[12:13]
	v_lshl_add_u64 v[0:1], s[30:31], 0, v[48:49]
	v_lshlrev_b32_e32 v4, 1, v2
	v_add_u32_e32 v14, 32, v12
	v_ashrrev_i32_e32 v16, 3, v68
	v_lshl_add_u64 v[18:19], v[0:1], 0, v[4:5]
	s_waitcnt lgkmcnt(0)
	s_barrier
; __device__ __forceinline__ int v_st(int k, int c) { const int kk = (k & ~0xC) | ((k & 4) << 1) | ((k & 8) >> 1); return ((kk >> 3) * 4 + (c >> 5)) * 512 + ((kk & 7) * 32 + (c & 31)) * 2; }
; __device__ __forceinline__ int v_rd_base(int lane) { return ((lane & 3) << 3) | (((lane >> 2) & 3) << 6) | (((lane >> 4) & 1) << 5) | (((lane >> 5) & 1) << 8); }
; #define SLOAD(k0) do { vs0 = *reinterpret_cast<const bf16x8*>(&Vh[(size_t)((k0) + sr) * DM + sc]); vs1 = *reinterpret_cast<const bf16x8*>(&Vh[(size_t)((k0) + 32 + sr) * DM + sc]); \
;     ks = *reinterpret_cast<const bf16x8*>(&Kh[(size_t)((k0) + kr) * DM + kc]); } while (0)
; #define SWRITE(s) do { *(bf16x8*)(V_lds + (s) * SHM_V + vst0) = vs0; *(bf16x8*)(V_lds + (s) * SHM_V + vst1) = vs1; *(bf16x8*)(K_lds + (s) * SHM_K64 + kst) = ks; } while (0)
; #define EX2(x) x = __builtin_amdgcn_exp2f(x)
; __device__ __forceinline__ void diff_pass(const bf16_t* __restrict__ Qb, const bf16_t* __restrict__ Kh, const bf16_t* __restrict__ Vh, int seq, char* lds, f32x16 (&o)[4], const int wave_) {
;     ...
;     const int sr = tid >> 4, sc = (tid & 15) * 8, vst0 = v_st(sr, sc), vst1 = v_st(32 + sr, sc);
;     const int kr = tid >> 3, kc = (tid & 7) * 8, kst = kswz<64>(kr, kc * 2);
;     const int vb0 = (int)(uintptr_t)V_lds + v_rd_base(lane);
;     bf16x8 vs0, vs1, ks;
;     ...
;     f32x16 pA0, pA1, pB0, pB1, negm; float alA, alB; bf16x8 pa0, pa1, pa2, pa3; const int NT = seq / 64;
;     int s_prev = 0, s_cur = 0, s_next = 1;
;     __syncthreads();
;     SLOAD(0); SWRITE(0); SLOAD(64); __syncthreads();
;     negm = f32x16{};
;     qkt64c(pA0, pA1, K_lds, qr, negm, r32, hi);
;     { const float pm = rowmax32(pA0, pA1); m_reg = pm; alA = 1.f;
; #pragma unroll
;       for (int r = 0; r < 16; ++r) { pA0[r] -= pm; pA1[r] -= pm; negm[r] = -pm; }
; #pragma unroll
;       for (int r = 0; r < 16; ++r) EX2(pA0[r]);
; #pragma unroll
;       for (int r = 0; r < 8; ++r) EX2(pA1[r]); }
;     SWRITE(1); __syncthreads();
	v_ashrrev_i32_e32 v15, 31, v14
	v_ashrrev_i32_e32 v17, 31, v16
	v_lshlrev_b32_e32 v64, 4, v68
	v_lshlrev_b64 v[6:7], 11, v[14:15]
	v_lshlrev_b64 v[50:51], 11, v[16:17]
	v_lshl_add_u64 v[6:7], s[30:31], 0, v[6:7]
	v_and_b32_e32 v20, 0x70, v64
	v_lshl_add_u64 v[8:9], s[28:29], 0, v[50:51]
	v_mov_b32_e32 v21, v161
	v_lshl_add_u64 v[4:5], v[6:7], 0, v[4:5]
	v_lshl_add_u64 v[22:23], v[8:9], 0, v[20:21]
	v_and_b32_e32 v13, 0xfffff0, v12
	v_lshlrev_b32_e32 v15, 1, v12
	v_and_or_b32 v13, v15, 8, v13
	v_lshrrev_b32_e32 v15, 1, v12
	v_lshrrev_b32_e32 v13, 1, v13
	v_bfe_u32 v17, v24, 5, 2
	v_and_b32_e32 v12, 3, v12
	v_or_b32_e32 v13, v13, v17
	v_and_or_b32 v12, v15, 4, v12
	v_lshlrev_b32_e32 v13, 9, v13
	v_lshlrev_b32_e32 v12, 6, v12
	v_and_b32_e32 v15, 48, v64
	v_or3_b32 v222, v13, v12, v15
	v_and_b32_e32 v13, 0xfffff0, v14
	v_lshlrev_b32_e32 v14, 1, v14
	v_and_or_b32 v13, v14, 8, v13
	v_lshrrev_b32_e32 v13, 1, v13
	v_or_b32_e32 v13, v13, v17
	v_add_u32_e32 v70, 0, v222
	s_mov_b32 s0, 0x20000
	v_lshlrev_b32_e32 v13, 9, v13
	v_or3_b32 v223, v13, v12, v15
	v_lshlrev_b32_e32 v12, 7, v16
	v_and_b32_e32 v13, 0x70, v68
	s_mov_b32 s1, 0x30000
	v_bitop3_b32 v224, v20, v12, v13 bitop3:0xde
	v_add_u32_e32 v71, 0, v223
	v_add_u32_e32 v225, 0, v224
	v_and_b32_e32 v69, 31, v68
	v_lshlrev_b32_e32 v12, 7, v69
	v_and_b32_e32 v13, 0x70, v24
	v_bitop3_b32 v227, v160, v12, v13 bitop3:0xde
	v_add_u32_e32 v226, 0, v227
	v_and_b32_e32 v72, 63, v68
	s_mov_b32 s12, 0
	s_mov_b32 s13, s12
	s_mov_b32 s14, s12
	s_mov_b32 s15, s12
	s_mov_b32 s16, s12
	s_mov_b32 s17, s12
	s_mov_b32 s18, s12
	s_mov_b32 s19, s12
	s_mov_b32 s20, s12
	s_mov_b32 s21, s12
	s_mov_b32 s22, s12
	s_mov_b32 s23, s12
	s_mov_b32 s24, s12
	s_mov_b32 s25, s12
	s_mov_b32 s26, s12
	s_mov_b32 s27, s12
	s_cmp_lg_u32 0, -1
	s_mov_b32 s29, 2
	s_mov_b32 s28, -1
	s_mov_b32 s30, 1
	v_mov_b32_e32 v234, 1.0
	v_mov_b32_e32 v219, 0
	s_waitcnt vmcnt(0)
	ds_write_b128 v70, v[178:181]
	v_add_co_u32_e32 v0, vcc, s0, v18
	s_nop 1
	v_addc_co_u32_e32 v1, vcc, 0, v19, vcc
	global_load_dwordx4 v[52:55], v[0:1], off
	v_add_co_u32_e32 v0, vcc, s1, v18
	s_waitcnt vmcnt(2)
	ds_write_b128 v71, v[182:185]
	v_addc_co_u32_e32 v1, vcc, 0, v19, vcc
	s_waitcnt vmcnt(1)
	ds_write_b128 v225, v[186:189] offset:49152
	v_add_co_u32_e32 v2, vcc, s0, v22
	v_and_b32_e32 v8, 0x3fffffc0, v68
	s_nop 0
	v_addc_co_u32_e32 v3, vcc, 0, v23, vcc
	global_load_dwordx4 v[56:59], v[0:1], off
	global_load_dwordx4 v[60:63], v[2:3], off offset:128
	s_waitcnt lgkmcnt(0)
	s_barrier
	ds_read_b128 v[0:3], v226 offset:49152
	ds_read_b128 v[4:7], v226 offset:53248
	s_waitcnt lgkmcnt(1)
	v_mfma_f32_32x32x16_bf16 v[32:47], v[0:3], v[162:165], 0
	v_or_b32_e32 v0, 32, v160
	v_bitop3_b32 v231, v0, v12, v13 bitop3:0xde
	v_add_u32_e32 v228, 0, v231
	v_lshl_add_u32 v217, v8, 2, s39
	s_cselect_b32 s0, 0, 0
	v_lshl_add_u32 v218, v69, 2, v217
	s_waitcnt lgkmcnt(0)
	v_mfma_f32_32x32x16_bf16 v[16:31], v[4:7], v[162:165], 0
	ds_read_b128 v[0:3], v228 offset:49152
	ds_read_b128 v[4:7], v228 offset:53248
	s_waitcnt lgkmcnt(1)
	v_mfma_f32_32x32x16_bf16 v[32:47], v[0:3], v[166:169], v[32:47]
	v_or_b32_e32 v0, 64, v160
	v_bitop3_b32 v232, v0, v12, v13 bitop3:0xde
	v_add_u32_e32 v229, 0, v232
	ds_read_b128 v[0:3], v229 offset:53248
	ds_read_b128 v[8:11], v229 offset:49152
	s_waitcnt lgkmcnt(2)
	v_mfma_f32_32x32x16_bf16 v[16:31], v[4:7], v[166:169], v[16:31]
	v_lshlrev_b32_e32 v4, 3, v72
	v_and_b32_e32 v5, 0xc0, v64
	v_lshlrev_b32_e32 v6, 1, v68
	v_and_or_b32 v5, v4, 24, v5
	v_and_b32_e32 v6, 32, v6
	v_and_b32_e32 v4, 0x100, v4
	v_or3_b32 v220, v5, v6, v4
	s_waitcnt lgkmcnt(0)
	v_mfma_f32_32x32x16_bf16 v[32:47], v[8:11], v[170:173], v[32:47]
	v_or_b32_e32 v4, 0x60, v160
	v_bitop3_b32 v233, v4, v12, v13 bitop3:0xde
	v_add_u32_e32 v230, 0, v233
	ds_read_b128 v[64:67], v230 offset:53248
	ds_read_b128 v[4:7], v230 offset:49152
	s_waitcnt vmcnt(2)
	ds_write_b128 v70, v[52:55] offset:16384
	s_waitcnt vmcnt(1)
	ds_write_b128 v71, v[56:59] offset:16384
	s_waitcnt vmcnt(0)
	ds_write_b128 v225, v[60:63] offset:57344
	v_mfma_f32_32x32x16_bf16 v[16:31], v[0:3], v[170:173], v[16:31]
	v_add_u32_e32 v221, s0, v220
	v_cmp_gt_u32_e64 s[0:1], 32, v72
	s_waitcnt lgkmcnt(0)
	s_barrier
; __device__ __forceinline__ int v_st(int k, int c) { const int kk = (k & ~0xC) | ((k & 4) << 1) | ((k & 8) >> 1); return ((kk >> 3) * 4 + (c >> 5)) * 512 + ((kk & 7) * 32 + (c & 31)) * 2; }
; __device__ __forceinline__ int v_rd_base(int lane) { return ((lane & 3) << 3) | (((lane >> 2) & 3) << 6) | (((lane >> 4) & 1) << 5) | (((lane >> 5) & 1) << 8); }
; #define EX2(x) x = __builtin_amdgcn_exp2f(x)
; __device__ __forceinline__ void diff_pass(const bf16_t* __restrict__ Qb, const bf16_t* __restrict__ Kh, const bf16_t* __restrict__ Vh, int seq, char* lds, f32x16 (&o)[4], const int wave_) {
;     ...
;     const int sr = tid >> 4, sc = (tid & 15) * 8, vst0 = v_st(sr, sc), vst1 = v_st(32 + sr, sc);
;     const int kr = tid >> 3, kc = (tid & 7) * 8, kst = kswz<64>(kr, kc * 2);
;     const int vb0 = (int)(uintptr_t)V_lds + v_rd_base(lane);
;     bf16x8 vs0, vs1, ks;
;     ...
;     { const float pm = rowmax32(pA0, pA1); m_reg = pm; alA = 1.f;
; #pragma unroll
;       for (int r = 0; r < 16; ++r) { pA0[r] -= pm; pA1[r] -= pm; negm[r] = -pm; }
; #pragma unroll
;       for (int r = 0; r < 16; ++r) EX2(pA0[r]);
; #pragma unroll
;       for (int r = 0; r < 8; ++r) EX2(pA1[r]); }
	v_mfma_f32_32x32x16_bf16 v[32:47], v[4:7], v[174:177], v[32:47]
	v_mov_b64_e32 v[0:1], s[12:13]
	v_mov_b64_e32 v[14:15], s[26:27]
	v_mov_b64_e32 v[2:3], s[14:15]
	v_mov_b64_e32 v[4:5], s[16:17]
	v_mov_b64_e32 v[6:7], s[18:19]
	v_mov_b64_e32 v[8:9], s[20:21]
	v_mov_b64_e32 v[10:11], s[22:23]
	v_mfma_f32_32x32x16_bf16 v[16:31], v[64:67], v[174:177], v[16:31]
	s_nop 3
	v_max_f32_e32 v64, v33, v33
	v_max_f32_e32 v65, v32, v32
	v_max_f32_e32 v64, v65, v64
	v_mov_b64_e32 v[12:13], s[24:25]
	s_nop 3
	v_max3_f32 v65, v34, v35, v17
	v_max3_f32 v64, v64, v16, v18
	v_max3_f32 v64, v64, v19, v36
	v_max3_f32 v65, v65, v38, v39
	v_max3_f32 v64, v64, v37, v20
	v_max3_f32 v65, v65, v22, v23
	v_max3_f32 v64, v64, v21, v40
	v_max3_f32 v65, v65, v42, v43
	v_max3_f32 v64, v64, v41, v24
	v_max3_f32 v65, v65, v26, v27
	v_max3_f32 v64, v64, v25, v44
	v_max3_f32 v65, v65, v46, v47
	v_max3_f32 v64, v64, v45, v28
	v_max3_f32 v65, v65, v30, v31
	v_max3_f32 v64, v64, v29, v65
	v_mov_b32_e32 v65, v64
	s_nop 1
	v_permlane32_swap_b32_e32 v64, v65
	v_max_f32_e32 v65, v65, v65
	v_max_f32_e32 v64, v64, v64
	v_max_f32_e32 v196, v64, v65
	v_sub_f32_e32 v18, v18, v196
	v_sub_f32_e32 v16, v16, v196
	v_sub_f32_e32 v17, v17, v196
	v_sub_f32_e32 v19, v19, v196
	v_exp_f32_e32 v114, v18
	v_and_b32_e32 v18, 7, v68
	v_exp_f32_e32 v112, v16
	v_exp_f32_e32 v113, v17
	v_exp_f32_e32 v115, v19
	v_lshl_add_u64 v[16:17], s[10:11], 0, v[50:51]
	v_lshlrev_b32_e32 v18, 4, v18
	v_mov_b32_e32 v19, v161
	v_sub_f32_e32 v32, v32, v196
	v_sub_f32_e32 v33, v33, v196
	v_sub_f32_e32 v34, v34, v196
	v_sub_f32_e32 v35, v35, v196
	v_sub_f32_e32 v36, v36, v196
	v_sub_f32_e32 v20, v20, v196
	v_sub_f32_e32 v37, v37, v196
	v_sub_f32_e32 v21, v21, v196
	v_sub_f32_e32 v38, v38, v196
	v_sub_f32_e32 v22, v22, v196
	v_sub_f32_e32 v39, v39, v196
	v_sub_f32_e32 v23, v23, v196
	v_sub_f32_e32 v40, v40, v196
	v_sub_f32_e32 v41, v41, v196
	v_pk_add_f32 v[120:121], v[24:25], v[196:197] op_sel_hi:[1,0] neg_lo:[0,1] neg_hi:[0,1]
	v_sub_f32_e32 v24, v42, v196
	v_sub_f32_e32 v25, v43, v196
	v_pk_add_f32 v[122:123], v[26:27], v[196:197] op_sel_hi:[1,0] neg_lo:[0,1] neg_hi:[0,1]
	v_sub_f32_e32 v26, v44, v196
	v_sub_f32_e32 v27, v45, v196
	v_pk_add_f32 v[124:125], v[28:29], v[196:197] op_sel_hi:[1,0] neg_lo:[0,1] neg_hi:[0,1]
	v_sub_f32_e32 v28, v46, v196
	v_sub_f32_e32 v29, v47, v196
	v_lshl_add_u64 v[16:17], v[16:17], 0, v[18:19]
	v_and_b32_e32 v18, 15, v68
	v_exp_f32_e32 v96, v32
	v_exp_f32_e32 v97, v33
	v_exp_f32_e32 v98, v34
	v_exp_f32_e32 v99, v35
	v_exp_f32_e32 v100, v36
	v_exp_f32_e32 v101, v37
	v_exp_f32_e32 v102, v38
	v_exp_f32_e32 v103, v39
	v_exp_f32_e32 v104, v40
	v_exp_f32_e32 v105, v41
	v_exp_f32_e32 v106, v24
	v_exp_f32_e32 v107, v25
	v_exp_f32_e32 v108, v26
	v_exp_f32_e32 v109, v27
	v_exp_f32_e32 v110, v28
	v_exp_f32_e32 v111, v29
	v_exp_f32_e32 v116, v20
	v_exp_f32_e32 v117, v21
	v_exp_f32_e32 v118, v22
	v_exp_f32_e32 v119, v23
	v_lshl_add_u64 v[198:199], s[52:53], 0, v[16:17]
	v_lshl_add_u64 v[16:17], s[10:11], 0, v[48:49]
	v_lshlrev_b32_e32 v18, 4, v18
	v_lshl_add_u64 v[16:17], v[16:17], 0, v[18:19]
	v_xor_b32_e32 v80, 0x80000000, v196
	v_pk_add_f32 v[126:127], v[30:31], v[196:197] op_sel_hi:[1,0] neg_lo:[0,1] neg_hi:[0,1]
	v_lshl_add_u64 v[200:201], s[52:53], 0, v[16:17]
	s_add_u32 s14, s52, s10
	s_addc_u32 s15, s53, s11
	s_add_u32 s14, s14, s64
	s_addc_u32 s15, s15, s65
	s_add_u32 s16, s14, 0x8a40000
	s_addc_u32 s17, s15, 0
	s_add_u32 s14, s14, 0x6a40080
	s_addc_u32 s15, s15, 0
	s_lshl_b32 s18, s55, 4
	v_lshrrev_b32_e32 v194, 4, v207
	v_xor_b32_e32 v194, v194, v207
	v_and_b32_e32 v194, 7, v194
	v_lshrrev_b32_e32 v195, 3, v207
	v_lshlrev_b32_e32 v195, 11, v195
	v_lshl_or_b32 v194, v194, 4, v195
	v_lshrrev_b32_e32 v195, 2, v207
	v_and_b32_e32 v195, 7, v195
	v_and_b32_e32 v255, 3, v195
	v_lshrrev_b32_e32 v195, 2, v195
	v_lshl_or_b32 v255, v195, 3, v255
	v_lshrrev_b32_e32 v195, 7, v207
	v_and_b32_e32 v195, 1, v195
	v_lshl_or_b32 v255, v195, 2, v255
	v_lshrrev_b32_e32 v195, 8, v207
	v_lshl_or_b32 v255, v195, 4, v255
	v_lshlrev_b32_e32 v255, 11, v255
	v_lshrrev_b32_e32 v195, 5, v207
	v_and_b32_e32 v195, 3, v195
	v_lshl_or_b32 v255, v195, 6, v255
	v_and_b32_e32 v195, 3, v207
	v_lshl_or_b32 v195, v195, 4, v255
	v_add_u32_e32 v255, 0x10000, v195
	v_mov_b64_e32 v[62:63], v[14:15]
	v_mov_b64_e32 v[46:47], v[14:15]
	v_mov_b64_e32 v[30:31], v[14:15]
	v_mov_b64_e32 v[60:61], v[12:13]
	v_mov_b64_e32 v[58:59], v[10:11]
	v_mov_b64_e32 v[56:57], v[8:9]
	v_mov_b64_e32 v[54:55], v[6:7]
	v_mov_b64_e32 v[52:53], v[4:5]
	v_mov_b64_e32 v[50:51], v[2:3]
	v_mov_b64_e32 v[48:49], v[0:1]
	v_mov_b64_e32 v[44:45], v[12:13]
	v_mov_b64_e32 v[42:43], v[10:11]
	v_mov_b64_e32 v[40:41], v[8:9]
	v_mov_b64_e32 v[38:39], v[6:7]
	v_mov_b64_e32 v[36:37], v[4:5]
	v_mov_b64_e32 v[34:35], v[2:3]
	v_mov_b64_e32 v[32:33], v[0:1]
	v_mov_b64_e32 v[28:29], v[12:13]
	v_mov_b64_e32 v[26:27], v[10:11]
	v_mov_b64_e32 v[24:25], v[8:9]
	v_mov_b64_e32 v[22:23], v[6:7]
	v_mov_b64_e32 v[20:21], v[4:5]
	v_mov_b64_e32 v[18:19], v[2:3]
	v_mov_b64_e32 v[16:17], v[0:1]
	v_mov_b32_e32 v81, v80
	v_mov_b32_e32 v82, v80
	v_mov_b32_e32 v83, v80
	v_mov_b32_e32 v84, v80
	v_mov_b32_e32 v85, v80
	v_mov_b32_e32 v86, v80
	v_mov_b32_e32 v87, v80
	v_mov_b32_e32 v88, v80
	v_mov_b32_e32 v89, v80
	v_mov_b32_e32 v90, v80
	v_mov_b32_e32 v91, v80
	v_mov_b32_e32 v92, v80
	v_mov_b32_e32 v93, v80
	v_mov_b32_e32 v94, v80
	v_mov_b32_e32 v95, v80

; #define SBAR() __builtin_amdgcn_sched_barrier(0)
; #define SLOAD(k0) do { vs0 = *reinterpret_cast<const bf16x8*>(&Vh[(size_t)((k0) + sr) * DM + sc]); vs1 = *reinterpret_cast<const bf16x8*>(&Vh[(size_t)((k0) + 32 + sr) * DM + sc]); \
;     ks = *reinterpret_cast<const bf16x8*>(&Kh[(size_t)((k0) + kr) * DM + kc]); } while (0)
; __device__ __forceinline__ void diff_pass(const bf16_t* __restrict__ Qb, const bf16_t* __restrict__ Kh, const bf16_t* __restrict__ Vh, int seq, char* lds, f32x16 (&o)[4], const int wave_) {
;     ...
;         SLOAD((j + 1) * 64);
;         SBAR(); qkt64c(pB0, pB1, K_lds + s_cur * SHM_K64, qr, negm, r32, hi); FIN(pA0, pA1, alA); SBAR();
;         YSEG(pB0, pB1, alB, s_prev);
.Latt9_p2_top:
	ds_read_b128 v[144:147], v128 offset:49152
	ds_read_b128 v[148:151], v129 offset:49152
	ds_read_b128 v[152:155], v130 offset:49152
	ds_read_b128 v[156:159], v131 offset:49152
	ds_read_b128 v[190:193], v128 offset:53248
	ds_read_b128 v[236:239], v129 offset:53248
	ds_read_b128 v[240:243], v130 offset:53248
	ds_read_b128 v[244:247], v131 offset:53248
	s_lshl_b32 s19, s29, 14
	s_add_i32 s19, s19, s18
	s_mov_b32 m0, s19
	s_lshl_b32 s20, s29, 13
	global_load_lds_dwordx4 v195, s[16:17]
	s_add_i32 m0, s19, 0x2000
	s_add_i32 s20, s20, s18
	global_load_lds_dwordx4 v255, s[16:17]
	s_add_i32 m0, s20, 0xc000
	s_add_u32 s16, s16, 0x20000
	global_load_lds_dwordx4 v194, s[14:15]
	s_addc_u32 s17, s17, 0
	s_add_u32 s14, s14, 0x20000
	s_addc_u32 s15, s15, 0
	v_exp_f32_e32 v208, v120
	v_exp_f32_e32 v209, v121
	v_add_f32_e32 v120, v96, v97
	v_add_f32_e32 v121, v98, v99
	s_waitcnt lgkmcnt(7)
	v_mfma_f32_32x32x16_bf16 v[128:143], v[144:147], v[162:165], v[80:95]
	v_exp_f32_e32 v210, v122
	v_add_f32_e32 v120, v120, v121
	v_add_f32_e32 v121, v100, v101
	v_add_f32_e32 v122, v102, v103
	v_exp_f32_e32 v211, v123
	s_waitcnt lgkmcnt(6)
	v_mfma_f32_32x32x16_bf16 v[128:143], v[148:151], v[166:169], v[128:143]
	v_add_f32_e32 v121, v121, v122
	v_add_f32_e32 v122, v104, v105
	v_add_f32_e32 v123, v106, v107
	v_add_f32_e32 v122, v122, v123
	v_add_f32_e32 v123, v108, v109
	s_waitcnt lgkmcnt(5)
	v_mfma_f32_32x32x16_bf16 v[128:143], v[152:155], v[170:173], v[128:143]
	v_exp_f32_e32 v124, v124
	v_exp_f32_e32 v125, v125
	v_exp_f32_e32 v126, v126
	v_exp_f32_e32 v127, v127
	v_cvt_pk_bf16_f32 v96, v96, v97
	s_waitcnt lgkmcnt(4)
	v_mfma_f32_32x32x16_bf16 v[128:143], v[156:159], v[174:177], v[128:143]
	v_cvt_pk_bf16_f32 v97, v98, v99
	v_cvt_pk_bf16_f32 v98, v100, v101
	v_cvt_pk_bf16_f32 v99, v102, v103
	s_nop 0
	v_permlane32_swap_b32_e32 v96, v98
	s_waitcnt lgkmcnt(3)
	v_mfma_f32_32x32x16_bf16 v[144:159], v[190:193], v[162:165], v[80:95]
	v_add_f32_e32 v190, v110, v111
	v_add_f32_e32 v123, v123, v190
	v_add_f32_e32 v190, v112, v113
	v_add_f32_e32 v191, v114, v115
	v_add_f32_e32 v190, v190, v191
	v_add_f32_e32 v120, v190, v120
	v_add_f32_e32 v190, v116, v117
	s_waitcnt lgkmcnt(2)
	v_mfma_f32_32x32x16_bf16 v[144:159], v[236:239], v[166:169], v[144:159]
	v_lshl_add_u32 v238, s12, 14, v221
	ds_read_b64_tr_b16 v[64:65], v238 offset:0
	ds_read_b64_tr_b16 v[66:67], v238 offset:0x800
	ds_read_b64_tr_b16 v[68:69], v238 offset:0x1000
	ds_read_b64_tr_b16 v[70:71], v238 offset:0x1800
	ds_read_b64_tr_b16 v[72:73], v238 offset:0x2000
	ds_read_b64_tr_b16 v[74:75], v238 offset:0x2800
	ds_read_b64_tr_b16 v[76:77], v238 offset:0x3000
	ds_read_b64_tr_b16 v[78:79], v238 offset:0x3800
	v_add_f32_e32 v191, v118, v119
	v_add_f32_e32 v190, v190, v191
	v_add_f32_e32 v121, v190, v121
	v_add_f32_e32 v190, v208, v209
	v_add_f32_e32 v191, v210, v211
	v_add_f32_e32 v190, v190, v191
	v_add_f32_e32 v122, v122, v190
	s_waitcnt lgkmcnt(9)
	v_mfma_f32_32x32x16_bf16 v[144:159], v[240:243], v[170:173], v[144:159]
	v_add_f32_e32 v190, v124, v125
	v_add_f32_e32 v191, v126, v127
	v_add_f32_e32 v190, v190, v191
	v_add_f32_e32 v123, v123, v190
	v_add_f32_e32 v120, v120, v121
	v_add_f32_e32 v121, v122, v123
	v_add_f32_e32 v235, v120, v121
	s_waitcnt lgkmcnt(8)
	v_mfma_f32_32x32x16_bf16 v[144:159], v[244:247], v[174:177], v[144:159]
	v_mov_b32_e32 v236, v235
	v_cvt_pk_bf16_f32 v120, v104, v105
	v_cvt_pk_bf16_f32 v121, v106, v107
	v_cvt_pk_bf16_f32 v122, v108, v109
	v_cvt_pk_bf16_f32 v123, v110, v111
	v_permlane32_swap_b32_e32 v97, v99
	v_cvt_pk_bf16_f32 v104, v112, v113
	v_cvt_pk_bf16_f32 v105, v114, v115
	v_cvt_pk_bf16_f32 v106, v116, v117
	v_cvt_pk_bf16_f32 v107, v118, v119
	s_waitcnt lgkmcnt(0)
	v_mfma_f32_32x32x16_bf16 v[0:15], v[96:99], v[64:67], v[0:15]
	v_permlane32_swap_b32_e32 v120, v122
	v_permlane32_swap_b32_e32 v121, v123
	v_cvt_pk_bf16_f32 v100, v208, v209
	v_cvt_pk_bf16_f32 v101, v210, v211
	v_cvt_pk_bf16_f32 v102, v124, v125
	v_cvt_pk_bf16_f32 v103, v126, v127
	v_mfma_f32_32x32x16_bf16 v[0:15], v[120:123], v[68:71], v[0:15]
	v_permlane32_swap_b32_e32 v104, v106
	v_permlane32_swap_b32_e32 v105, v107
	ds_read_b64_tr_b16 v[190:191], v238 offset:0x200
	ds_read_b64_tr_b16 v[192:193], v238 offset:0xa00
	ds_read_b64_tr_b16 v[240:241], v238 offset:0x1200
	ds_read_b64_tr_b16 v[242:243], v238 offset:0x1a00
	ds_read_b64_tr_b16 v[244:245], v238 offset:0x2200
	ds_read_b64_tr_b16 v[246:247], v238 offset:0x2a00
	ds_read_b64_tr_b16 v[208:209], v238 offset:0x3200
	ds_read_b64_tr_b16 v[210:211], v238 offset:0x3a00
	v_mfma_f32_32x32x16_bf16 v[0:15], v[104:107], v[72:75], v[0:15]
	v_permlane32_swap_b32_e32 v100, v102
	v_permlane32_swap_b32_e32 v101, v103
	v_permlane32_swap_b32_e32 v235, v236
	v_max_f32_e32 v108, v128, v129
	v_max3_f32 v108, v108, v144, v146
	v_max3_f32 v109, v130, v131, v145
	v_max3_f32 v108, v108, v147, v132
	v_max3_f32 v109, v109, v134, v135
	v_mfma_f32_32x32x16_bf16 v[0:15], v[100:103], v[76:79], v[0:15]
	v_max3_f32 v237, v108, v133, v148
	v_max3_f32 v239, v109, v150, v151
	ds_read_b64_tr_b16 v[124:125], v238 offset:0x400
	ds_read_b64_tr_b16 v[126:127], v238 offset:0xc00
	ds_read_b64_tr_b16 v[116:117], v238 offset:0x1400
	ds_read_b64_tr_b16 v[118:119], v238 offset:0x1c00
	ds_read_b64_tr_b16 v[112:113], v238 offset:0x2400
	ds_read_b64_tr_b16 v[114:115], v238 offset:0x2c00
	ds_read_b64_tr_b16 v[108:109], v238 offset:0x3400
	ds_read_b64_tr_b16 v[110:111], v238 offset:0x3c00
	s_waitcnt lgkmcnt(8)
	v_mfma_f32_32x32x16_bf16 v[48:63], v[96:99], v[190:193], v[48:63]
	v_max3_f32 v190, v237, v149, v136
	v_max3_f32 v191, v239, v138, v139
	v_max3_f32 v190, v190, v137, v152
	v_max3_f32 v191, v191, v154, v155
	v_max3_f32 v190, v190, v153, v140
	v_max3_f32 v191, v191, v142, v143
	v_max3_f32 v190, v190, v141, v156
	v_mfma_f32_32x32x16_bf16 v[48:63], v[120:123], v[240:243], v[48:63]
	v_max3_f32 v191, v191, v158, v159
	v_max3_f32 v190, v190, v157, v191
	v_mov_b32_e32 v191, v190
	s_nop 1
	v_permlane32_swap_b32_e32 v190, v191
	v_mfma_f32_32x32x16_bf16 v[48:63], v[104:107], v[244:247], v[48:63]
	v_max_f32_e32 v237, v190, v191
	s_mov_b32 s2, 0x4138aa3b
	v_cmp_ge_f32_e32 vcc, s2, v237
	v_mfma_f32_32x32x16_bf16 v[48:63], v[100:103], v[208:211], v[48:63]
	s_cmp_eq_u64 vcc, exec
	s_cbranch_scc0 .LBB0_859
	v_mov_b32_e32 v237, 1.0
; #define SBAR() __builtin_amdgcn_sched_barrier(0)
; #define SLOAD(k0) do { vs0 = *reinterpret_cast<const bf16x8*>(&Vh[(size_t)((k0) + sr) * DM + sc]); vs1 = *reinterpret_cast<const bf16x8*>(&Vh[(size_t)((k0) + 32 + sr) * DM + sc]); \
;     ks = *reinterpret_cast<const bf16x8*>(&Kh[(size_t)((k0) + kr) * DM + kc]); } while (0)
; #define SWRITE(s) do { *(bf16x8*)(V_lds + (s) * SHM_V + vst0) = vs0; *(bf16x8*)(V_lds + (s) * SHM_V + vst1) = vs1; *(bf16x8*)(K_lds + (s) * SHM_K64 + kst) = ks; } while (0)
; #define RESC(a) do { if (__any((a) < 1.f)) { if (hi == 0) al_l[r32] = (a); asm volatile("s_waitcnt lgkmcnt(0)" ::: "memory"); \
;     _Pragma("unroll") for (int d = 0; d < 4; ++d) _Pragma("unroll") for (int r = 0; r < 16; ++r) o[d][r] *= al_l[crow(r, hi)]; } } while (0)
; #define ROT() do { s_prev = s_cur; s_cur = s_next; s_next = (s_next == DA_NBUF - 1) ? 0 : s_next + 1; } while (0)
; #define EX2(x) x = __builtin_amdgcn_exp2f(x)
; __device__ __forceinline__ void diff_pass(const bf16_t* __restrict__ Qb, const bf16_t* __restrict__ Kh, const bf16_t* __restrict__ Vh, int seq, char* lds, f32x16 (&o)[4], const int wave_) {
;     ...
;     f32x16 pA0, pA1, pB0, pB1, negm; float alA, alB; bf16x8 pa0, pa1, pa2, pa3; const int NT = seq / 64;
;     int s_prev = 0, s_cur = 0, s_next = 1;
;     __syncthreads();
;     SLOAD(0); SWRITE(0); SLOAD(64); __syncthreads();
;     negm = f32x16{};
;     qkt64c(pA0, pA1, K_lds, qr, negm, r32, hi);
;     { const float pm = rowmax32(pA0, pA1); m_reg = pm; alA = 1.f;
; #pragma unroll
;       for (int r = 0; r < 16; ++r) { pA0[r] -= pm; pA1[r] -= pm; negm[r] = -pm; }
; #pragma unroll
;       for (int r = 0; r < 16; ++r) EX2(pA0[r]);
; #pragma unroll
;       for (int r = 0; r < 8; ++r) EX2(pA1[r]); }
;     SWRITE(1); __syncthreads();
;     ROT();
;     for (int j = 1; j + 1 < NT; j += 2) {
;         SLOAD((j + 1) * 64);
;         SBAR(); qkt64c(pB0, pB1, K_lds + s_cur * SHM_K64, qr, negm, r32, hi); FIN(pA0, pA1, alA); SBAR();
;         YSEG(pB0, pB1, alB, s_prev);
;         SWRITE(s_next); RESC(alB); __syncthreads(); ROT();
;         SLOAD((j + 2) * 64);
;         SBAR(); qkt64c(pA0, pA1, K_lds + s_cur * SHM_K64, qr, negm, r32, hi); FIN(pB0, pB1, alB); SBAR();
.LBB0_848:
	ds_read_b64_tr_b16 v[190:191], v238 offset:0x600
	ds_read_b64_tr_b16 v[192:193], v238 offset:0xe00
	ds_read_b64_tr_b16 v[208:209], v238 offset:0x1600
	ds_read_b64_tr_b16 v[210:211], v238 offset:0x1e00
	ds_read_b64_tr_b16 v[240:241], v238 offset:0x2600
	ds_read_b64_tr_b16 v[242:243], v238 offset:0x2e00
	ds_read_b64_tr_b16 v[244:245], v238 offset:0x3600
	ds_read_b64_tr_b16 v[246:247], v238 offset:0x3e00
	s_waitcnt lgkmcnt(8)
	v_mfma_f32_32x32x16_bf16 v[32:47], v[96:99], v[124:127], v[32:47]
	v_exp_f32_e32 v128, v128
	v_exp_f32_e32 v129, v129
	v_exp_f32_e32 v130, v130
	v_mfma_f32_32x32x16_bf16 v[32:47], v[120:123], v[116:119], v[32:47]
	v_exp_f32_e32 v131, v131
	v_exp_f32_e32 v132, v132
	v_exp_f32_e32 v133, v133
	v_mfma_f32_32x32x16_bf16 v[32:47], v[104:107], v[112:115], v[32:47]
	v_exp_f32_e32 v134, v134
	v_exp_f32_e32 v135, v135
	v_exp_f32_e32 v136, v136
	v_mfma_f32_32x32x16_bf16 v[32:47], v[100:103], v[108:111], v[32:47]
	v_exp_f32_e32 v137, v137
	v_exp_f32_e32 v138, v138
	v_exp_f32_e32 v139, v139
	s_waitcnt lgkmcnt(0)
	s_lshl_b32 s2, s29, 14
	s_add_i32 s2, s2, 0
	s_lshl_b32 s3, s29, 13
	s_sub_i32 s2, s2, s3
	v_mfma_f32_32x32x16_bf16 v[16:31], v[96:99], v[190:193], v[16:31]
	v_exp_f32_e32 v140, v140
	v_exp_f32_e32 v141, v141
	v_exp_f32_e32 v142, v142
	v_mfma_f32_32x32x16_bf16 v[16:31], v[120:123], v[208:211], v[16:31]
	v_exp_f32_e32 v143, v143
	v_exp_f32_e32 v144, v144
	v_exp_f32_e32 v145, v145
	v_cmp_gt_f32_e32 vcc, 1.0, v237
	v_mfma_f32_32x32x16_bf16 v[16:31], v[104:107], v[240:243], v[16:31]
	v_exp_f32_e32 v146, v146
	v_exp_f32_e32 v147, v147
	v_exp_f32_e32 v148, v148
	v_mfma_f32_32x32x16_bf16 v[16:31], v[100:103], v[244:247], v[16:31]
	v_exp_f32_e32 v149, v149
	v_exp_f32_e32 v150, v150
	v_exp_f32_e32 v151, v151
	s_cbranch_vccz .LBB0_852
	s_and_saveexec_b64 s[10:11], s[0:1]
	ds_write_b32 v218, v237 offset:128
	s_or_b64 exec, exec, s[10:11]
	s_waitcnt lgkmcnt(0)
	v_add_u32_e32 v108, v217, v160
	ds_read_b128 v[96:99], v108 offset:224
	ds_read_b128 v[100:103], v108 offset:192
	ds_read_b128 v[104:107], v108 offset:160
	ds_read_b128 v[108:111], v108 offset:128
	s_waitcnt lgkmcnt(3)
	v_pk_mul_f32 v[12:13], v[12:13], v[96:97]
	s_waitcnt lgkmcnt(2)
	v_pk_mul_f32 v[8:9], v[8:9], v[100:101]
	s_waitcnt lgkmcnt(1)
	v_pk_mul_f32 v[4:5], v[4:5], v[104:105]
	v_pk_mul_f32 v[14:15], v[14:15], v[98:99]
	v_pk_mul_f32 v[10:11], v[10:11], v[102:103]
	v_pk_mul_f32 v[6:7], v[6:7], v[106:107]
	s_waitcnt lgkmcnt(0)
	v_pk_mul_f32 v[2:3], v[2:3], v[110:111]
	v_pk_mul_f32 v[0:1], v[0:1], v[108:109]
	v_pk_mul_f32 v[60:61], v[60:61], v[96:97]
	v_pk_mul_f32 v[56:57], v[56:57], v[100:101]
	v_pk_mul_f32 v[52:53], v[52:53], v[104:105]
	v_pk_mul_f32 v[62:63], v[62:63], v[98:99]
	v_pk_mul_f32 v[58:59], v[58:59], v[102:103]
	v_pk_mul_f32 v[54:55], v[54:55], v[106:107]
	v_pk_mul_f32 v[50:51], v[50:51], v[110:111]
	v_pk_mul_f32 v[48:49], v[48:49], v[108:109]
	v_pk_mul_f32 v[44:45], v[44:45], v[96:97]
	v_pk_mul_f32 v[40:41], v[40:41], v[100:101]
	v_pk_mul_f32 v[36:37], v[36:37], v[104:105]
	v_pk_mul_f32 v[46:47], v[46:47], v[98:99]
	v_pk_mul_f32 v[42:43], v[42:43], v[102:103]
	v_pk_mul_f32 v[38:39], v[38:39], v[106:107]
	v_pk_mul_f32 v[34:35], v[34:35], v[110:111]
	v_pk_mul_f32 v[32:33], v[32:33], v[108:109]
	v_pk_mul_f32 v[28:29], v[28:29], v[96:97]
	v_pk_mul_f32 v[24:25], v[24:25], v[100:101]
	v_pk_mul_f32 v[20:21], v[20:21], v[104:105]
	v_pk_mul_f32 v[30:31], v[30:31], v[98:99]
	v_pk_mul_f32 v[26:27], v[26:27], v[102:103]
	v_pk_mul_f32 v[22:23], v[22:23], v[106:107]
	v_pk_mul_f32 v[18:19], v[18:19], v[110:111]
	v_pk_mul_f32 v[16:17], v[16:17], v[108:109]
.LBB0_852:
	s_waitcnt lgkmcnt(0)
	v_add_u32_e32 v102, s2, v227
	v_add_u32_e32 v103, s2, v231
	v_add_u32_e32 v104, s2, v232
	v_add_u32_e32 v105, s2, v233
	s_waitcnt vmcnt(0)
	s_barrier
	ds_read_b128 v[112:115], v102 offset:49152
	ds_read_b128 v[116:119], v103 offset:49152
	ds_read_b128 v[120:123], v104 offset:49152
	ds_read_b128 v[124:127], v105 offset:49152
	ds_read_b128 v[190:193], v102 offset:53248
	ds_read_b128 v[202:205], v103 offset:53248
	ds_read_b128 v[208:211], v104 offset:53248
	ds_read_b128 v[238:241], v105 offset:53248
	s_add_i32 s3, s29, 1
	s_cmp_lg_u32 s29, 2
	s_cselect_b32 s3, s3, 0
	s_lshl_b32 s19, s3, 14
	s_add_i32 s19, s19, s18
	s_mov_b32 m0, s19
	s_lshl_b32 s20, s3, 13
	global_load_lds_dwordx4 v195, s[16:17]
	s_add_i32 m0, s19, 0x2000
	s_add_i32 s20, s20, s18
	global_load_lds_dwordx4 v255, s[16:17]
	s_add_i32 m0, s20, 0xc000
	s_add_u32 s16, s16, 0x20000
	global_load_lds_dwordx4 v194, s[14:15]
	s_addc_u32 s17, s17, 0
	s_add_u32 s14, s14, 0x20000
	s_addc_u32 s15, s15, 0
	v_exp_f32_e32 v242, v152
	v_exp_f32_e32 v243, v153
	v_add_f32_e32 v152, v128, v129
	v_add_f32_e32 v153, v130, v131
	s_waitcnt lgkmcnt(7)
	v_mfma_f32_32x32x16_bf16 v[96:111], v[112:115], v[162:165], v[80:95]
	v_exp_f32_e32 v244, v154
	v_add_f32_e32 v152, v152, v153
	v_add_f32_e32 v153, v132, v133
	v_add_f32_e32 v154, v134, v135
	v_exp_f32_e32 v245, v155
	s_waitcnt lgkmcnt(6)
	v_mfma_f32_32x32x16_bf16 v[96:111], v[116:119], v[166:169], v[96:111]
	v_add_f32_e32 v153, v153, v154
	v_add_f32_e32 v154, v136, v137
	v_add_f32_e32 v155, v138, v139
	v_add_f32_e32 v154, v154, v155
	v_add_f32_e32 v155, v140, v141
	s_waitcnt lgkmcnt(5)
	v_mfma_f32_32x32x16_bf16 v[96:111], v[120:123], v[170:173], v[96:111]
	v_exp_f32_e32 v156, v156
	v_exp_f32_e32 v157, v157
	v_exp_f32_e32 v158, v158
	v_exp_f32_e32 v159, v159
	s_waitcnt lgkmcnt(4)
	v_mfma_f32_32x32x16_bf16 v[96:111], v[124:127], v[174:177], v[96:111]
	s_waitcnt lgkmcnt(3)
	v_mfma_f32_32x32x16_bf16 v[112:127], v[190:193], v[162:165], v[80:95]
	v_add_f32_e32 v190, v142, v143
	v_add_f32_e32 v155, v155, v190
	v_add_f32_e32 v190, v144, v145
	v_add_f32_e32 v191, v146, v147
	v_add_f32_e32 v190, v190, v191
	v_add_f32_e32 v152, v152, v190
	v_add_f32_e32 v190, v148, v149
	s_waitcnt lgkmcnt(2)
	v_mfma_f32_32x32x16_bf16 v[112:127], v[202:205], v[166:169], v[112:127]
	v_lshl_add_u32 v205, s30, 14, v221
	ds_read_b64_tr_b16 v[64:65], v205 offset:0
	ds_read_b64_tr_b16 v[66:67], v205 offset:0x800
	ds_read_b64_tr_b16 v[68:69], v205 offset:0x1000
	ds_read_b64_tr_b16 v[70:71], v205 offset:0x1800
	ds_read_b64_tr_b16 v[72:73], v205 offset:0x2000
	ds_read_b64_tr_b16 v[74:75], v205 offset:0x2800
	ds_read_b64_tr_b16 v[76:77], v205 offset:0x3000
	ds_read_b64_tr_b16 v[78:79], v205 offset:0x3800
	v_add_f32_e32 v191, v150, v151
	v_add_f32_e32 v190, v190, v191
	v_add_f32_e32 v153, v153, v190
	v_add_f32_e32 v190, v242, v243
	v_add_f32_e32 v191, v244, v245
	v_add_f32_e32 v190, v190, v191
	v_add_f32_e32 v154, v154, v190
	s_waitcnt lgkmcnt(9)
	v_mfma_f32_32x32x16_bf16 v[112:127], v[208:211], v[170:173], v[112:127]
	v_add_f32_e32 v190, v156, v157
	v_add_f32_e32 v191, v158, v159
	v_add_f32_e32 v190, v190, v191
	v_add_f32_e32 v155, v155, v190
	v_add_f32_e32 v152, v152, v153
	v_add_f32_e32 v153, v154, v155
	v_add_f32_e32 v203, v152, v153
	s_waitcnt lgkmcnt(8)
	v_mfma_f32_32x32x16_bf16 v[112:127], v[238:241], v[174:177], v[112:127]
	v_mov_b32_e32 v204, v203
	v_cvt_pk_bf16_f32 v152, v128, v129
	v_cvt_pk_bf16_f32 v153, v130, v131
	v_cvt_pk_bf16_f32 v154, v132, v133
	v_cvt_pk_bf16_f32 v155, v134, v135
	v_cvt_pk_bf16_f32 v136, v136, v137
	v_cvt_pk_bf16_f32 v137, v138, v139
	v_cvt_pk_bf16_f32 v138, v140, v141
	v_cvt_pk_bf16_f32 v139, v142, v143
	v_permlane32_swap_b32_e32 v152, v154
	v_permlane32_swap_b32_e32 v153, v155
	v_cvt_pk_bf16_f32 v132, v144, v145
	v_cvt_pk_bf16_f32 v133, v146, v147
	v_cvt_pk_bf16_f32 v134, v148, v149
	v_cvt_pk_bf16_f32 v135, v150, v151
	s_waitcnt lgkmcnt(0)
	v_mfma_f32_32x32x16_bf16 v[0:15], v[152:155], v[64:67], v[0:15]
	v_permlane32_swap_b32_e32 v136, v138
	v_permlane32_swap_b32_e32 v137, v139
	v_cvt_pk_bf16_f32 v128, v242, v243
	v_cvt_pk_bf16_f32 v129, v244, v245
	v_cvt_pk_bf16_f32 v130, v156, v157
	v_cvt_pk_bf16_f32 v131, v158, v159
	v_mfma_f32_32x32x16_bf16 v[0:15], v[136:139], v[68:71], v[0:15]
	v_permlane32_swap_b32_e32 v132, v134
	v_permlane32_swap_b32_e32 v133, v135
	ds_read_b64_tr_b16 v[190:191], v205 offset:0x200
	ds_read_b64_tr_b16 v[192:193], v205 offset:0xa00
	ds_read_b64_tr_b16 v[208:209], v205 offset:0x1200
	ds_read_b64_tr_b16 v[210:211], v205 offset:0x1a00
	ds_read_b64_tr_b16 v[238:239], v205 offset:0x2200
	ds_read_b64_tr_b16 v[240:241], v205 offset:0x2a00
	ds_read_b64_tr_b16 v[242:243], v205 offset:0x3200
	ds_read_b64_tr_b16 v[244:245], v205 offset:0x3a00
	v_mfma_f32_32x32x16_bf16 v[0:15], v[132:135], v[72:75], v[0:15]
	v_permlane32_swap_b32_e32 v128, v130
	v_permlane32_swap_b32_e32 v129, v131
	v_permlane32_swap_b32_e32 v203, v204
	v_max_f32_e32 v140, v96, v97
	v_max3_f32 v140, v140, v112, v114
	v_max3_f32 v141, v98, v99, v113
	v_max3_f32 v140, v140, v115, v100
	v_max3_f32 v141, v141, v102, v103
	v_mfma_f32_32x32x16_bf16 v[0:15], v[128:131], v[76:79], v[0:15]
	v_max3_f32 v202, v140, v101, v116
	v_max3_f32 v246, v141, v118, v119
	ds_read_b64_tr_b16 v[156:157], v205 offset:0x400
	ds_read_b64_tr_b16 v[158:159], v205 offset:0xc00
	ds_read_b64_tr_b16 v[148:149], v205 offset:0x1400
	ds_read_b64_tr_b16 v[150:151], v205 offset:0x1c00
	ds_read_b64_tr_b16 v[144:145], v205 offset:0x2400
	ds_read_b64_tr_b16 v[146:147], v205 offset:0x2c00
	ds_read_b64_tr_b16 v[140:141], v205 offset:0x3400
	ds_read_b64_tr_b16 v[142:143], v205 offset:0x3c00
	s_waitcnt lgkmcnt(8)
	v_mfma_f32_32x32x16_bf16 v[48:63], v[152:155], v[190:193], v[48:63]
	v_max3_f32 v190, v202, v117, v104
	v_max3_f32 v191, v246, v106, v107
	v_max3_f32 v190, v190, v105, v120
	v_max3_f32 v191, v191, v122, v123
	v_max3_f32 v190, v190, v121, v108
	v_max3_f32 v191, v191, v110, v111
	v_max3_f32 v190, v190, v109, v124
	v_mfma_f32_32x32x16_bf16 v[48:63], v[136:139], v[208:211], v[48:63]
	v_max3_f32 v191, v191, v126, v127
	v_max3_f32 v190, v190, v125, v191
	v_mov_b32_e32 v191, v190
	s_nop 1
	v_permlane32_swap_b32_e32 v190, v191
	v_mfma_f32_32x32x16_bf16 v[48:63], v[132:135], v[238:241], v[48:63]
	v_max_f32_e32 v238, v190, v191
	s_mov_b32 s2, 0x4138aa3b
	v_cmp_ge_f32_e32 vcc, s2, v238
	v_mfma_f32_32x32x16_bf16 v[48:63], v[128:131], v[242:245], v[48:63]
	s_cmp_eq_u64 vcc, exec
	v_mov_b32_e32 v202, 1.0
	s_cbranch_scc0 .LBB0_860
.LBB0_853:
	ds_read_b64_tr_b16 v[190:191], v205 offset:0x600
	ds_read_b64_tr_b16 v[192:193], v205 offset:0xe00
	ds_read_b64_tr_b16 v[208:209], v205 offset:0x1600
	ds_read_b64_tr_b16 v[210:211], v205 offset:0x1e00
	ds_read_b64_tr_b16 v[238:239], v205 offset:0x2600
	ds_read_b64_tr_b16 v[240:241], v205 offset:0x2e00
	ds_read_b64_tr_b16 v[242:243], v205 offset:0x3600
	ds_read_b64_tr_b16 v[244:245], v205 offset:0x3e00
	s_add_i32 s2, s29, 1
	s_waitcnt lgkmcnt(8)
	s_cmp_lg_u32 s29, 2
	s_cselect_b32 s30, s2, 0
	v_mfma_f32_32x32x16_bf16 v[32:47], v[152:155], v[156:159], v[32:47]
	v_exp_f32_e32 v96, v96
	v_exp_f32_e32 v97, v97
	v_exp_f32_e32 v98, v98
	v_mfma_f32_32x32x16_bf16 v[32:47], v[136:139], v[148:151], v[32:47]
	v_exp_f32_e32 v99, v99
	v_exp_f32_e32 v100, v100
	v_exp_f32_e32 v101, v101
	v_mfma_f32_32x32x16_bf16 v[32:47], v[132:135], v[144:147], v[32:47]
	v_exp_f32_e32 v102, v102
	v_exp_f32_e32 v103, v103
	v_exp_f32_e32 v104, v104
	v_mfma_f32_32x32x16_bf16 v[32:47], v[128:131], v[140:143], v[32:47]
	v_exp_f32_e32 v105, v105
	v_exp_f32_e32 v106, v106
	v_exp_f32_e32 v107, v107
	s_waitcnt lgkmcnt(0)
	s_lshl_b32 s2, s30, 14
	s_add_i32 s2, s2, 0
	v_mfma_f32_32x32x16_bf16 v[16:31], v[152:155], v[190:193], v[16:31]
	v_exp_f32_e32 v108, v108
	v_exp_f32_e32 v109, v109
	v_exp_f32_e32 v110, v110
	v_mfma_f32_32x32x16_bf16 v[16:31], v[136:139], v[208:211], v[16:31]
	v_exp_f32_e32 v111, v111
	v_exp_f32_e32 v112, v112
	v_exp_f32_e32 v113, v113
	v_cmp_gt_f32_e32 vcc, 1.0, v202
	v_mfma_f32_32x32x16_bf16 v[16:31], v[132:135], v[238:241], v[16:31]
	v_exp_f32_e32 v114, v114
	v_exp_f32_e32 v115, v115
	v_exp_f32_e32 v116, v116
	v_mfma_f32_32x32x16_bf16 v[16:31], v[128:131], v[242:245], v[16:31]
	v_exp_f32_e32 v117, v117
	v_exp_f32_e32 v118, v118
	v_exp_f32_e32 v119, v119
	s_cbranch_vccz .LBB0_857
	s_and_saveexec_b64 s[10:11], s[0:1]
	ds_write_b32 v218, v202 offset:128
	s_or_b64 exec, exec, s[10:11]
	s_waitcnt lgkmcnt(0)
	v_add_u32_e32 v140, v217, v160
	ds_read_b128 v[128:131], v140 offset:224
	ds_read_b128 v[132:135], v140 offset:192
	ds_read_b128 v[136:139], v140 offset:160
	ds_read_b128 v[140:143], v140 offset:128
	s_waitcnt lgkmcnt(3)
	v_pk_mul_f32 v[12:13], v[12:13], v[128:129]
	s_waitcnt lgkmcnt(2)
	v_pk_mul_f32 v[8:9], v[8:9], v[132:133]
	s_waitcnt lgkmcnt(1)
	v_pk_mul_f32 v[4:5], v[4:5], v[136:137]
	v_pk_mul_f32 v[14:15], v[14:15], v[130:131]
	v_pk_mul_f32 v[10:11], v[10:11], v[134:135]
	v_pk_mul_f32 v[6:7], v[6:7], v[138:139]
	s_waitcnt lgkmcnt(0)
	v_pk_mul_f32 v[2:3], v[2:3], v[142:143]
	v_pk_mul_f32 v[0:1], v[0:1], v[140:141]
	v_pk_mul_f32 v[60:61], v[60:61], v[128:129]
	v_pk_mul_f32 v[56:57], v[56:57], v[132:133]
	v_pk_mul_f32 v[52:53], v[52:53], v[136:137]
	v_pk_mul_f32 v[62:63], v[62:63], v[130:131]
	v_pk_mul_f32 v[58:59], v[58:59], v[134:135]
	v_pk_mul_f32 v[54:55], v[54:55], v[138:139]
	v_pk_mul_f32 v[50:51], v[50:51], v[142:143]
	v_pk_mul_f32 v[48:49], v[48:49], v[140:141]
	v_pk_mul_f32 v[44:45], v[44:45], v[128:129]
	v_pk_mul_f32 v[40:41], v[40:41], v[132:133]
	v_pk_mul_f32 v[36:37], v[36:37], v[136:137]
	v_pk_mul_f32 v[46:47], v[46:47], v[130:131]
	v_pk_mul_f32 v[42:43], v[42:43], v[134:135]
	v_pk_mul_f32 v[38:39], v[38:39], v[138:139]
	v_pk_mul_f32 v[34:35], v[34:35], v[142:143]
	v_pk_mul_f32 v[32:33], v[32:33], v[140:141]
	v_pk_mul_f32 v[28:29], v[28:29], v[128:129]
	v_pk_mul_f32 v[24:25], v[24:25], v[132:133]
	v_pk_mul_f32 v[20:21], v[20:21], v[136:137]
	v_pk_mul_f32 v[30:31], v[30:31], v[130:131]
	v_pk_mul_f32 v[26:27], v[26:27], v[134:135]
	v_pk_mul_f32 v[22:23], v[22:23], v[138:139]
	v_pk_mul_f32 v[18:19], v[18:19], v[142:143]
	v_pk_mul_f32 v[16:17], v[16:17], v[140:141]
.LBB0_857:
	s_add_i32 s2, s30, 1
	v_add_f32_e32 v128, v235, v236
	s_cmp_lg_u32 s30, 2
	v_fmac_f32_e32 v128, v219, v234
	v_add_f32_e32 v219, v203, v204
	s_cselect_b32 s2, s2, 0
	s_add_i32 s28, s28, 2
	v_fmac_f32_e32 v219, v128, v237
	s_lshl_b32 s3, s30, 13
	s_cmp_gt_u32 s28, 28
	v_add_u32_e32 v128, s3, v227
	v_add_u32_e32 v129, s3, v231
	v_add_u32_e32 v130, s3, v232
	v_add_u32_e32 v131, s3, v233
	v_mov_b32_e32 v234, v202
	s_mov_b32 s12, s29
	s_mov_b32 s29, s2
	s_waitcnt lgkmcnt(0)
	s_waitcnt vmcnt(0)
	s_barrier
	s_cbranch_scc1 .LBB0_861
	s_branch .Latt9_p2_top
